# attention: K/V fragment LDS reads software-pipelined through register rings (QK and PV), on top of quad handoff + residual epilogues
# speedup vs baseline: 1.0137x; 1.0022x over previous
.Lqo_p4b2:
	s_bfe_i32 s1, s0, 0x80000
	s_bfe_u32 s1, s1, 0x5000a
	s_add_i32 s1, s0, s1
	s_bfe_i32 s1, s1, 0x80000
	s_sext_i32_i16 s1, s1
	s_ashr_i32 s13, s1, 5
	s_lshl_b32 s1, s13, 2
	s_add_i32 s2, s1, s12
	s_ashr_i32 s3, s2, 31
	s_lshl_b64 s[2:3], s[2:3], 17
	s_add_u32 s8, s58, s2
	s_addc_u32 s1, s59, s3
	s_and_b32 s9, s1, 0xffff
	s_ashr_i32 s1, s0, 31
	s_lshl_b64 s[0:1], s[0:1], 8
	v_lshl_add_u64 v[96:97], s[0:1], 0, v[128:129]
	s_lshl_b32 s0, s12, 8
	s_ashr_i32 s1, s0, 31
	s_lshl_b64 s[2:3], s[0:1], 1
	s_waitcnt vmcnt(0)
	v_lshl_add_u64 v[98:99], v[132:133], 0, s[2:3]
	v_lshlrev_b64 v[138:139], 11, v[96:97]
	s_waitcnt lgkmcnt(0)
	s_barrier
	v_lshl_add_u64 v[4:5], v[98:99], 0, v[138:139]
	global_load_dwordx4 v[64:67], v[4:5], off
	global_load_dwordx4 v[68:71], v[4:5], off offset:64
	global_load_dwordx4 v[72:75], v[4:5], off offset:128
	global_load_dwordx4 v[76:79], v[4:5], off offset:192
	global_load_dwordx4 v[80:83], v[4:5], off offset:256
	global_load_dwordx4 v[84:87], v[4:5], off offset:320
	global_load_dwordx4 v[88:91], v[4:5], off offset:384
	global_load_dwordx4 v[92:95], v[4:5], off offset:448
	v_add_u32_e32 v188, v150, v151
	v_add_u32_e32 v187, v150, v152
	v_add_u32_e32 v186, v150, v153
	v_add_u32_e32 v137, v150, v154
	v_add_u32_e32 v135, v150, v151
	v_add_u32_e32 v135, 0x10000, v135
	v_add_u32_e32 v159, v150, v152
	v_add_u32_e32 v159, 0x10000, v159
	v_add_u32_e32 v176, v150, v153
	v_add_u32_e32 v176, 0x10000, v176
	v_add_u32_e32 v177, v150, v154
	v_add_u32_e32 v177, 0x10000, v177
	ds_read_b128 v[100:103], v188
	ds_read_b128 v[160:163], v187
	ds_read_b128 v[164:167], v186
	ds_read_b128 v[168:171], v137
	ds_read_b128 v[172:175], v188 offset:256
	ds_read_b128 v[204:207], v187 offset:256
	ds_read_b128 v[208:211], v186 offset:256
	ds_read_b128 v[212:215], v137 offset:256
	s_mov_b32 s11, s10
	s_mov_b32 m0, s29
	s_add_i32 s20, s20, s38
	s_ashr_i32 s0, s20, 31
	s_lshr_b32 s0, s0, 25
	s_add_i32 s0, s20, s0
	s_ashr_i32 s1, s0, 7
	s_and_b32 s0, s0, 0xff80
	s_sub_i32 s0, s20, s0
	s_cmp_eq_u32 s100, 1
	s_cbranch_scc0 .Lqo_p4b3
	s_mov_b32 s1, s99
	s_lshr_b32 s0, s20, 8
	s_add_i32 s0, s0, s98
	s_add_i32 s0, s0, s98
.Lqo_p4b3:
	s_waitcnt vmcnt(7)
	s_waitcnt lgkmcnt(7)
	v_mfma_f32_16x16x32_bf16 v[4:7], v[100:103], v[64:67], 0
	ds_read_b128 v[248:251], v188 offset:8192
	s_waitcnt vmcnt(6)
	s_waitcnt lgkmcnt(7)
	v_mfma_f32_16x16x32_bf16 v[4:7], v[160:163], v[68:71], v[4:7]
	ds_read_b128 v[252:255], v187 offset:8192
	s_waitcnt vmcnt(5)
	s_waitcnt lgkmcnt(7)
	v_mfma_f32_16x16x32_bf16 v[4:7], v[164:167], v[72:75], v[4:7]
	ds_read_b128 v[100:103], v186 offset:8192
	s_waitcnt vmcnt(4)
	s_waitcnt lgkmcnt(7)
	v_mfma_f32_16x16x32_bf16 v[4:7], v[168:171], v[76:79], v[4:7]
	ds_read_b128 v[160:163], v137 offset:8192
	s_waitcnt vmcnt(3)
	s_waitcnt lgkmcnt(7)
	v_mfma_f32_16x16x32_bf16 v[4:7], v[172:175], v[80:83], v[4:7]
	ds_read_b128 v[164:167], v188 offset:8448
	s_waitcnt vmcnt(2)
	s_waitcnt lgkmcnt(7)
	v_mfma_f32_16x16x32_bf16 v[4:7], v[204:207], v[84:87], v[4:7]
	ds_read_b128 v[168:171], v187 offset:8448
	s_waitcnt vmcnt(1)
	s_waitcnt lgkmcnt(7)
	v_mfma_f32_16x16x32_bf16 v[4:7], v[208:211], v[88:91], v[4:7]
	ds_read_b128 v[172:175], v186 offset:8448
	s_waitcnt vmcnt(0)
	s_waitcnt lgkmcnt(7)
	v_mfma_f32_16x16x32_bf16 v[4:7], v[212:215], v[92:95], v[4:7]
	ds_read_b128 v[204:207], v137 offset:8448
	s_waitcnt lgkmcnt(7)
	v_mfma_f32_16x16x32_bf16 v[8:11], v[248:251], v[64:67], 0
	ds_read_b128 v[208:211], v188 offset:16384
	s_waitcnt lgkmcnt(7)
	v_mfma_f32_16x16x32_bf16 v[8:11], v[252:255], v[68:71], v[8:11]
	ds_read_b128 v[212:215], v187 offset:16384
	s_waitcnt lgkmcnt(7)
	v_mfma_f32_16x16x32_bf16 v[8:11], v[100:103], v[72:75], v[8:11]
	ds_read_b128 v[248:251], v186 offset:16384
	s_waitcnt lgkmcnt(7)
	v_mfma_f32_16x16x32_bf16 v[8:11], v[160:163], v[76:79], v[8:11]
	ds_read_b128 v[252:255], v137 offset:16384
	s_waitcnt lgkmcnt(7)
	v_mfma_f32_16x16x32_bf16 v[8:11], v[164:167], v[80:83], v[8:11]
	ds_read_b128 v[100:103], v188 offset:16640
	s_waitcnt lgkmcnt(7)
	v_mfma_f32_16x16x32_bf16 v[8:11], v[168:171], v[84:87], v[8:11]
	ds_read_b128 v[160:163], v187 offset:16640
	s_waitcnt lgkmcnt(7)
	v_mfma_f32_16x16x32_bf16 v[8:11], v[172:175], v[88:91], v[8:11]
	ds_read_b128 v[164:167], v186 offset:16640
	s_waitcnt lgkmcnt(7)
	v_mfma_f32_16x16x32_bf16 v[12:15], v[204:207], v[92:95], v[8:11]
	ds_read_b128 v[168:171], v137 offset:16640
	s_nop 4
	s_waitcnt lgkmcnt(7)
	v_mfma_f32_16x16x32_bf16 v[8:11], v[208:211], v[64:67], 0
	ds_read_b128 v[172:175], v188 offset:24576
	s_waitcnt lgkmcnt(7)
	v_mfma_f32_16x16x32_bf16 v[8:11], v[212:215], v[68:71], v[8:11]
	ds_read_b128 v[204:207], v187 offset:24576
	s_waitcnt lgkmcnt(7)
	v_mfma_f32_16x16x32_bf16 v[8:11], v[248:251], v[72:75], v[8:11]
	ds_read_b128 v[208:211], v186 offset:24576
	s_waitcnt lgkmcnt(7)
	v_mfma_f32_16x16x32_bf16 v[8:11], v[252:255], v[76:79], v[8:11]
	ds_read_b128 v[212:215], v137 offset:24576
	s_waitcnt lgkmcnt(7)
	v_mfma_f32_16x16x32_bf16 v[8:11], v[100:103], v[80:83], v[8:11]
	ds_read_b128 v[248:251], v188 offset:24832
	s_waitcnt lgkmcnt(7)
	v_mfma_f32_16x16x32_bf16 v[8:11], v[160:163], v[84:87], v[8:11]
	ds_read_b128 v[252:255], v187 offset:24832
	s_waitcnt lgkmcnt(7)
	v_mfma_f32_16x16x32_bf16 v[8:11], v[164:167], v[88:91], v[8:11]
	ds_read_b128 v[100:103], v186 offset:24832
	s_waitcnt lgkmcnt(7)
	v_mfma_f32_16x16x32_bf16 v[8:11], v[168:171], v[92:95], v[8:11]
	ds_read_b128 v[160:163], v137 offset:24832
	s_waitcnt lgkmcnt(7)
	v_mfma_f32_16x16x32_bf16 v[16:19], v[172:175], v[64:67], 0
	ds_read_b128 v[164:167], v188 offset:32768
	s_waitcnt lgkmcnt(7)
	v_mfma_f32_16x16x32_bf16 v[16:19], v[204:207], v[68:71], v[16:19]
	ds_read_b128 v[168:171], v187 offset:32768
	s_waitcnt lgkmcnt(7)
	v_mfma_f32_16x16x32_bf16 v[16:19], v[208:211], v[72:75], v[16:19]
	ds_read_b128 v[172:175], v186 offset:32768
	s_waitcnt lgkmcnt(7)
	v_mfma_f32_16x16x32_bf16 v[16:19], v[212:215], v[76:79], v[16:19]
	ds_read_b128 v[204:207], v137 offset:32768
	s_waitcnt lgkmcnt(7)
	v_mfma_f32_16x16x32_bf16 v[16:19], v[248:251], v[80:83], v[16:19]
	ds_read_b128 v[208:211], v188 offset:33024
	s_waitcnt lgkmcnt(7)
	v_mfma_f32_16x16x32_bf16 v[16:19], v[252:255], v[84:87], v[16:19]
	ds_read_b128 v[212:215], v187 offset:33024
	s_waitcnt lgkmcnt(7)
	v_mfma_f32_16x16x32_bf16 v[16:19], v[100:103], v[88:91], v[16:19]
	ds_read_b128 v[248:251], v186 offset:33024
	s_waitcnt lgkmcnt(7)
	v_mfma_f32_16x16x32_bf16 v[20:23], v[160:163], v[92:95], v[16:19]
	ds_read_b128 v[252:255], v137 offset:33024
	s_nop 4
	s_waitcnt lgkmcnt(7)
	v_mfma_f32_16x16x32_bf16 v[16:19], v[164:167], v[64:67], 0
	ds_read_b128 v[100:103], v188 offset:40960
	s_waitcnt lgkmcnt(7)
	v_mfma_f32_16x16x32_bf16 v[16:19], v[168:171], v[68:71], v[16:19]
	ds_read_b128 v[160:163], v187 offset:40960
	s_waitcnt lgkmcnt(7)
	v_mfma_f32_16x16x32_bf16 v[16:19], v[172:175], v[72:75], v[16:19]
	ds_read_b128 v[164:167], v186 offset:40960
	s_waitcnt lgkmcnt(7)
	v_mfma_f32_16x16x32_bf16 v[16:19], v[204:207], v[76:79], v[16:19]
	ds_read_b128 v[168:171], v137 offset:40960
	s_waitcnt lgkmcnt(7)
	v_mfma_f32_16x16x32_bf16 v[16:19], v[208:211], v[80:83], v[16:19]
	ds_read_b128 v[172:175], v188 offset:41216
	s_waitcnt lgkmcnt(7)
	v_mfma_f32_16x16x32_bf16 v[16:19], v[212:215], v[84:87], v[16:19]
	ds_read_b128 v[204:207], v187 offset:41216
	s_waitcnt lgkmcnt(7)
	v_mfma_f32_16x16x32_bf16 v[16:19], v[248:251], v[88:91], v[16:19]
	ds_read_b128 v[208:211], v186 offset:41216
	s_waitcnt lgkmcnt(7)
	v_mfma_f32_16x16x32_bf16 v[16:19], v[252:255], v[92:95], v[16:19]
	ds_read_b128 v[212:215], v137 offset:41216
	s_waitcnt lgkmcnt(7)
	v_mfma_f32_16x16x32_bf16 v[24:27], v[100:103], v[64:67], 0
	ds_read_b128 v[248:251], v188 offset:49152
	s_waitcnt lgkmcnt(7)
	v_mfma_f32_16x16x32_bf16 v[24:27], v[160:163], v[68:71], v[24:27]
	ds_read_b128 v[252:255], v187 offset:49152
	s_waitcnt lgkmcnt(7)
	v_mfma_f32_16x16x32_bf16 v[24:27], v[164:167], v[72:75], v[24:27]
	ds_read_b128 v[100:103], v186 offset:49152
	s_waitcnt lgkmcnt(7)
	v_mfma_f32_16x16x32_bf16 v[24:27], v[168:171], v[76:79], v[24:27]
	ds_read_b128 v[160:163], v137 offset:49152
	s_waitcnt lgkmcnt(7)
	v_mfma_f32_16x16x32_bf16 v[24:27], v[172:175], v[80:83], v[24:27]
	ds_read_b128 v[164:167], v188 offset:49408
	s_waitcnt lgkmcnt(7)
	v_mfma_f32_16x16x32_bf16 v[24:27], v[204:207], v[84:87], v[24:27]
	ds_read_b128 v[168:171], v187 offset:49408
	s_waitcnt lgkmcnt(7)
	v_mfma_f32_16x16x32_bf16 v[24:27], v[208:211], v[88:91], v[24:27]
	ds_read_b128 v[172:175], v186 offset:49408
	s_waitcnt lgkmcnt(7)
	v_mfma_f32_16x16x32_bf16 v[32:35], v[212:215], v[92:95], v[24:27]
	ds_read_b128 v[204:207], v137 offset:49408
	s_nop 4
	s_waitcnt lgkmcnt(7)
	v_mfma_f32_16x16x32_bf16 v[24:27], v[248:251], v[64:67], 0
	ds_read_b128 v[208:211], v188 offset:57344
	s_waitcnt lgkmcnt(7)
	v_mfma_f32_16x16x32_bf16 v[24:27], v[252:255], v[68:71], v[24:27]
	ds_read_b128 v[212:215], v187 offset:57344
	s_waitcnt lgkmcnt(7)
	v_mfma_f32_16x16x32_bf16 v[24:27], v[100:103], v[72:75], v[24:27]
	ds_read_b128 v[248:251], v186 offset:57344
	s_waitcnt lgkmcnt(7)
	v_mfma_f32_16x16x32_bf16 v[24:27], v[160:163], v[76:79], v[24:27]
	ds_read_b128 v[252:255], v137 offset:57344
	s_waitcnt lgkmcnt(7)
	v_mfma_f32_16x16x32_bf16 v[24:27], v[164:167], v[80:83], v[24:27]
	ds_read_b128 v[100:103], v188 offset:57600
	s_waitcnt lgkmcnt(7)
	v_mfma_f32_16x16x32_bf16 v[24:27], v[168:171], v[84:87], v[24:27]
	ds_read_b128 v[160:163], v187 offset:57600
	s_waitcnt lgkmcnt(7)
	v_mfma_f32_16x16x32_bf16 v[24:27], v[172:175], v[88:91], v[24:27]
	ds_read_b128 v[164:167], v186 offset:57600
	s_waitcnt lgkmcnt(7)
	v_mfma_f32_16x16x32_bf16 v[24:27], v[204:207], v[92:95], v[24:27]
	ds_read_b128 v[168:171], v137 offset:57600
	s_waitcnt lgkmcnt(7)
	v_mfma_f32_16x16x32_bf16 v[28:31], v[208:211], v[64:67], 0
	ds_read_b128 v[172:175], v135
	s_waitcnt lgkmcnt(7)
	v_mfma_f32_16x16x32_bf16 v[28:31], v[212:215], v[68:71], v[28:31]
	ds_read_b128 v[204:207], v159
	s_waitcnt lgkmcnt(7)
	v_mfma_f32_16x16x32_bf16 v[28:31], v[248:251], v[72:75], v[28:31]
	ds_read_b128 v[208:211], v176
	s_waitcnt lgkmcnt(7)
	v_mfma_f32_16x16x32_bf16 v[28:31], v[252:255], v[76:79], v[28:31]
	ds_read_b128 v[212:215], v177
	s_waitcnt lgkmcnt(7)
	v_mfma_f32_16x16x32_bf16 v[28:31], v[100:103], v[80:83], v[28:31]
	ds_read_b128 v[248:251], v135 offset:256
	s_waitcnt lgkmcnt(7)
	v_mfma_f32_16x16x32_bf16 v[28:31], v[160:163], v[84:87], v[28:31]
	ds_read_b128 v[252:255], v159 offset:256
	s_waitcnt lgkmcnt(7)
	v_mfma_f32_16x16x32_bf16 v[28:31], v[164:167], v[88:91], v[28:31]
	ds_read_b128 v[100:103], v176 offset:256
	s_waitcnt lgkmcnt(7)
	v_mfma_f32_16x16x32_bf16 v[36:39], v[168:171], v[92:95], v[28:31]
	ds_read_b128 v[160:163], v177 offset:256
	s_nop 4
	s_waitcnt lgkmcnt(7)
	v_mfma_f32_16x16x32_bf16 v[104:107], v[172:175], v[64:67], 0
	ds_read_b128 v[164:167], v135 offset:8192
	s_waitcnt lgkmcnt(7)
	v_mfma_f32_16x16x32_bf16 v[60:63], v[204:207], v[68:71], v[104:107]
	ds_read_b128 v[168:171], v159 offset:8192
	s_waitcnt lgkmcnt(7)
	v_mfma_f32_16x16x32_bf16 v[56:59], v[208:211], v[72:75], v[60:63]
	ds_read_b128 v[172:175], v176 offset:8192
	s_nop 2
	s_waitcnt lgkmcnt(7)
	v_mfma_f32_16x16x32_bf16 v[52:55], v[212:215], v[76:79], v[56:59]
	ds_read_b128 v[204:207], v177 offset:8192
	s_waitcnt lgkmcnt(7)
	v_mfma_f32_16x16x32_bf16 v[48:51], v[248:251], v[80:83], v[52:55]
	ds_read_b128 v[208:211], v135 offset:8448
	s_nop 2
	s_waitcnt lgkmcnt(7)
	v_mfma_f32_16x16x32_bf16 v[44:47], v[252:255], v[84:87], v[48:51]
	ds_read_b128 v[212:215], v159 offset:8448
	s_waitcnt lgkmcnt(7)
	v_mfma_f32_16x16x32_bf16 v[40:43], v[100:103], v[88:91], v[44:47]
	ds_read_b128 v[248:251], v176 offset:8448
	s_nop 1
	s_nop 3
	s_waitcnt lgkmcnt(7)
	v_mfma_f32_16x16x32_bf16 v[28:31], v[160:163], v[92:95], v[40:43]
	ds_read_b128 v[252:255], v177 offset:8448
	s_nop 2
	s_waitcnt lgkmcnt(7)
	v_mfma_f32_16x16x32_bf16 v[112:115], v[164:167], v[64:67], 0
	ds_read_b128 v[100:103], v135 offset:16384
	s_waitcnt lgkmcnt(7)
	v_mfma_f32_16x16x32_bf16 v[108:111], v[168:171], v[68:71], v[112:115]
	ds_read_b128 v[160:163], v159 offset:16384
	s_waitcnt lgkmcnt(7)
	v_mfma_f32_16x16x32_bf16 v[60:63], v[172:175], v[72:75], v[108:111]
	ds_read_b128 v[164:167], v176 offset:16384
	s_nop 4
	s_waitcnt lgkmcnt(7)
	v_mfma_f32_16x16x32_bf16 v[56:59], v[204:207], v[76:79], v[60:63]
	ds_read_b128 v[168:171], v177 offset:16384
	s_waitcnt lgkmcnt(7)
	v_mfma_f32_16x16x32_bf16 v[52:55], v[208:211], v[80:83], v[56:59]
	ds_read_b128 v[172:175], v135 offset:16640
	s_waitcnt lgkmcnt(7)
	v_mfma_f32_16x16x32_bf16 v[48:51], v[212:215], v[84:87], v[52:55]
	ds_read_b128 v[204:207], v159 offset:16640
	s_waitcnt lgkmcnt(7)
	v_mfma_f32_16x16x32_bf16 v[44:47], v[248:251], v[88:91], v[48:51]
	ds_read_b128 v[208:211], v176 offset:16640
	s_nop 3
	s_waitcnt lgkmcnt(7)
	v_mfma_f32_16x16x32_bf16 v[40:43], v[252:255], v[92:95], v[44:47]
	ds_read_b128 v[212:215], v177 offset:16640
	s_nop 2
	s_waitcnt lgkmcnt(7)
	v_mfma_f32_16x16x32_bf16 v[120:123], v[100:103], v[64:67], 0
	ds_read_b128 v[248:251], v135 offset:24576
	s_waitcnt lgkmcnt(7)
	v_mfma_f32_16x16x32_bf16 v[116:119], v[160:163], v[68:71], v[120:123]
	ds_read_b128 v[252:255], v159 offset:24576
	s_waitcnt lgkmcnt(7)
	v_mfma_f32_16x16x32_bf16 v[112:115], v[164:167], v[72:75], v[116:119]
	ds_read_b128 v[100:103], v176 offset:24576
	s_nop 5
	s_waitcnt lgkmcnt(7)
	v_mfma_f32_16x16x32_bf16 v[60:63], v[168:171], v[76:79], v[112:115]
	ds_read_b128 v[160:163], v177 offset:24576
	s_waitcnt lgkmcnt(7)
	v_mfma_f32_16x16x32_bf16 v[56:59], v[172:175], v[80:83], v[60:63]
	ds_read_b128 v[164:167], v135 offset:24832
	s_waitcnt lgkmcnt(7)
	v_mfma_f32_16x16x32_bf16 v[52:55], v[204:207], v[84:87], v[56:59]
	ds_read_b128 v[168:171], v135 offset:32768
	s_waitcnt lgkmcnt(7)
	v_mfma_f32_16x16x32_bf16 v[48:51], v[208:211], v[88:91], v[52:55]
	ds_read_b128 v[172:175], v159 offset:32768
	s_nop 1
	s_waitcnt lgkmcnt(7)
	v_mfma_f32_16x16x32_bf16 v[44:47], v[212:215], v[92:95], v[48:51]
	ds_read_b128 v[204:207], v159 offset:24832
	s_nop 2
	s_waitcnt lgkmcnt(7)
	v_mfma_f32_16x16x32_bf16 v[190:193], v[248:251], v[64:67], 0
	ds_read_b128 v[208:211], v176 offset:32768
	s_waitcnt lgkmcnt(7)
	v_mfma_f32_16x16x32_bf16 v[124:127], v[252:255], v[68:71], v[190:193]
	ds_read_b128 v[212:215], v177 offset:32768
	s_waitcnt lgkmcnt(7)
	v_mfma_f32_16x16x32_bf16 v[120:123], v[100:103], v[72:75], v[124:127]
	ds_read_b128 v[248:251], v135 offset:33024
	s_nop 5
	s_waitcnt lgkmcnt(7)
	v_mfma_f32_16x16x32_bf16 v[116:119], v[160:163], v[76:79], v[120:123]
	ds_read_b128 v[252:255], v159 offset:33024
	s_waitcnt lgkmcnt(7)
	v_mfma_f32_16x16x32_bf16 v[60:63], v[164:167], v[80:83], v[116:119]
	ds_read_b128 v[100:103], v135 offset:40960
	s_nop 0
	s_nop 3
	s_waitcnt lgkmcnt(7)
	v_mfma_f32_16x16x32_bf16 v[198:201], v[168:171], v[64:67], 0
	ds_read_b128 v[160:163], v176 offset:24832
	s_waitcnt lgkmcnt(7)
	v_mfma_f32_16x16x32_bf16 v[194:197], v[172:175], v[68:71], v[198:201]
	ds_read_b128 v[164:167], v159 offset:40960
	s_waitcnt lgkmcnt(7)
	v_mfma_f32_16x16x32_bf16 v[56:59], v[204:207], v[84:87], v[60:63]
	ds_read_b128 v[168:171], v177 offset:24832
	s_nop 3
	s_waitcnt lgkmcnt(7)
	v_mfma_f32_16x16x32_bf16 v[190:193], v[208:211], v[72:75], v[194:197]
	ds_read_b128 v[172:175], v176 offset:40960
	s_waitcnt lgkmcnt(7)
	v_mfma_f32_16x16x32_bf16 v[124:127], v[212:215], v[76:79], v[190:193]
	ds_read_b128 v[204:207], v177 offset:40960
	s_waitcnt lgkmcnt(7)
	v_mfma_f32_16x16x32_bf16 v[120:123], v[248:251], v[80:83], v[124:127]
	ds_read_b128 v[208:211], v176 offset:33024
	s_nop 1
	s_nop 2
	s_waitcnt lgkmcnt(7)
	v_mfma_f32_16x16x32_bf16 v[60:63], v[252:255], v[84:87], v[120:123]
	ds_read_b128 v[212:215], v135 offset:41216
	s_nop 2
	s_waitcnt lgkmcnt(7)
	v_mfma_f32_16x16x32_bf16 v[230:233], v[100:103], v[64:67], 0
	ds_read_b128 v[248:251], v177 offset:33024
	s_waitcnt lgkmcnt(7)
	v_mfma_f32_16x16x32_bf16 v[52:55], v[160:163], v[88:91], v[56:59]
	ds_read_b128 v[252:255], v135 offset:49152
	s_waitcnt lgkmcnt(7)
	v_mfma_f32_16x16x32_bf16 v[226:229], v[164:167], v[68:71], v[230:233]
	ds_read_b128 v[100:103], v159 offset:41216
	s_nop 1
	s_waitcnt lgkmcnt(7)
	v_mfma_f32_16x16x32_bf16 v[48:51], v[168:171], v[92:95], v[52:55]
	ds_read_b128 v[160:163], v159 offset:49152
	s_nop 2
	s_waitcnt lgkmcnt(7)
	v_mfma_f32_16x16x32_bf16 v[222:225], v[172:175], v[72:75], v[226:229]
	ds_read_b128 v[164:167], v176 offset:41216
	s_waitcnt lgkmcnt(7)
	v_mfma_f32_16x16x32_bf16 v[194:197], v[204:207], v[76:79], v[222:225]
	ds_read_b128 v[168:171], v176 offset:49152
	s_waitcnt lgkmcnt(7)
	v_mfma_f32_16x16x32_bf16 v[56:59], v[208:211], v[88:91], v[60:63]
	ds_read_b128 v[172:175], v177 offset:41216
	s_waitcnt lgkmcnt(7)
	v_mfma_f32_16x16x32_bf16 v[190:193], v[212:215], v[80:83], v[194:197]
	ds_read_b128 v[204:207], v177 offset:49152
	s_nop 1
	s_nop 1
	s_waitcnt lgkmcnt(7)
	v_mfma_f32_16x16x32_bf16 v[52:55], v[248:251], v[92:95], v[56:59]
	ds_read_b128 v[208:211], v135 offset:57344
	s_waitcnt lgkmcnt(7)
	v_mfma_f32_16x16x32_bf16 v[242:245], v[252:255], v[64:67], 0
	ds_read_b128 v[212:215], v135 offset:49408
	s_waitcnt lgkmcnt(7)
	v_mfma_f32_16x16x32_bf16 v[124:127], v[100:103], v[84:87], v[190:193]
	ds_read_b128 v[248:251], v159 offset:57344
	s_waitcnt lgkmcnt(7)
	v_mfma_f32_16x16x32_bf16 v[238:241], v[160:163], v[68:71], v[242:245]
	ds_read_b128 v[252:255], v159 offset:49408
	s_waitcnt lgkmcnt(7)
	v_mfma_f32_16x16x32_bf16 v[60:63], v[164:167], v[88:91], v[124:127]
	ds_read_b128 v[100:103], v176 offset:49408
	s_nop 4
	s_waitcnt lgkmcnt(7)
	v_mfma_f32_16x16x32_bf16 v[234:237], v[168:171], v[72:75], v[238:241]
	ds_read_b128 v[160:163], v177 offset:49408
	s_waitcnt lgkmcnt(7)
	v_mfma_f32_16x16x32_bf16 v[56:59], v[172:175], v[92:95], v[60:63]
	ds_read_b128 v[164:167], v176 offset:57344
	s_nop 2
	s_waitcnt lgkmcnt(7)
	v_mfma_f32_16x16x32_bf16 v[230:233], v[204:207], v[76:79], v[234:237]
	ds_read_b128 v[168:171], v177 offset:57344
	s_waitcnt lgkmcnt(7)
	v_mfma_f32_16x16x32_bf16 v[64:67], v[208:211], v[64:67], 0
	ds_read_b128 v[172:175], v135 offset:57600
	s_waitcnt lgkmcnt(7)
	v_mfma_f32_16x16x32_bf16 v[226:229], v[212:215], v[80:83], v[230:233]
	ds_read_b128 v[204:207], v159 offset:57600
	s_waitcnt lgkmcnt(7)
	v_mfma_f32_16x16x32_bf16 v[64:67], v[248:251], v[68:71], v[64:67]
	ds_read_b128 v[208:211], v176 offset:57600
	v_max_f32_e32 v68, v5, v5
	v_max_f32_e32 v69, v4, v4
	v_max_f32_e32 v68, v69, v68
	v_max_f32_e32 v69, v7, v7
	v_max_f32_e32 v70, v6, v6
	v_max_f32_e32 v69, v70, v69
	s_waitcnt lgkmcnt(7)
	v_mfma_f32_16x16x32_bf16 v[222:225], v[252:255], v[84:87], v[226:229]
	ds_read_b128 v[212:215], v177 offset:57600
	v_max3_f32 v68, v68, s61, v69
	v_max_f32_e32 v69, v13, v13
	v_max_f32_e32 v70, v12, v12
	v_max_f32_e32 v69, v70, v69
	v_max_f32_e32 v70, v15, v15
	v_max_f32_e32 v71, v14, v14
	v_max_f32_e32 v70, v71, v70
	v_max3_f32 v68, v68, v69, v70
	v_max_f32_e32 v69, v9, v9
	v_max_f32_e32 v70, v8, v8
	s_waitcnt lgkmcnt(7)
	v_mfma_f32_16x16x32_bf16 v[190:193], v[100:103], v[88:91], v[222:225]
	v_max_f32_e32 v69, v70, v69
	v_max_f32_e32 v70, v11, v11
	v_max_f32_e32 v71, v10, v10
	v_max_f32_e32 v70, v71, v70
	v_max3_f32 v68, v68, v69, v70
	v_max_f32_e32 v69, v21, v21
	v_max_f32_e32 v70, v20, v20
	v_max_f32_e32 v69, v70, v69
	v_max_f32_e32 v70, v23, v23
	v_max_f32_e32 v71, v22, v22
	s_waitcnt lgkmcnt(6)
	v_mfma_f32_16x16x32_bf16 v[60:63], v[160:163], v[92:95], v[190:193]
	v_max_f32_e32 v70, v71, v70
	v_max3_f32 v68, v68, v69, v70
	v_max_f32_e32 v69, v17, v17
	v_max_f32_e32 v70, v16, v16
	v_max_f32_e32 v69, v70, v69
	v_max_f32_e32 v70, v19, v19
	v_max_f32_e32 v71, v18, v18
	v_max_f32_e32 v70, v71, v70
	v_max3_f32 v68, v68, v69, v70
	v_max_f32_e32 v69, v33, v33
	v_max_f32_e32 v70, v32, v32
	v_max_f32_e32 v69, v70, v69
	v_max_f32_e32 v70, v35, v35
	v_max_f32_e32 v71, v34, v34
	v_max_f32_e32 v70, v71, v70
	v_max3_f32 v68, v68, v69, v70
	v_max_f32_e32 v69, v25, v25
	v_max_f32_e32 v70, v24, v24
	v_max_f32_e32 v69, v70, v69
	v_max_f32_e32 v70, v27, v27
	v_max_f32_e32 v71, v26, v26
	v_max_f32_e32 v70, v71, v70
	s_waitcnt lgkmcnt(5)
	v_mfma_f32_16x16x32_bf16 v[64:67], v[164:167], v[72:75], v[64:67]
	v_max3_f32 v68, v68, v69, v70
	v_max_f32_e32 v69, v37, v37
	v_max_f32_e32 v70, v36, v36
	v_max_f32_e32 v69, v70, v69
	v_max_f32_e32 v70, v39, v39
	v_max_f32_e32 v71, v38, v38
	v_max_f32_e32 v70, v71, v70
	v_max3_f32 v68, v68, v69, v70
	v_max_f32_e32 v69, v29, v29
	v_max_f32_e32 v70, v28, v28
	s_waitcnt lgkmcnt(4)
	v_mfma_f32_16x16x32_bf16 v[64:67], v[168:171], v[76:79], v[64:67]
	v_max_f32_e32 v69, v70, v69
	v_max_f32_e32 v70, v31, v31
	v_max_f32_e32 v71, v30, v30
	v_max_f32_e32 v70, v71, v70
	v_max3_f32 v68, v68, v69, v70
	v_max_f32_e32 v69, v41, v41
	v_max_f32_e32 v70, v40, v40
	v_max_f32_e32 v69, v70, v69
	v_max_f32_e32 v70, v43, v43
	v_max_f32_e32 v71, v42, v42
	s_waitcnt lgkmcnt(3)
	v_mfma_f32_16x16x32_bf16 v[64:67], v[172:175], v[80:83], v[64:67]
	v_max_f32_e32 v70, v71, v70
	v_max3_f32 v68, v68, v69, v70
	v_max_f32_e32 v69, v45, v45
	v_max_f32_e32 v70, v44, v44
	v_max_f32_e32 v69, v70, v69
	v_max_f32_e32 v70, v47, v47
	v_max_f32_e32 v71, v46, v46
	v_max_f32_e32 v70, v71, v70
	s_waitcnt lgkmcnt(2)
	v_mfma_f32_16x16x32_bf16 v[64:67], v[204:207], v[84:87], v[64:67]
	v_max3_f32 v68, v68, v69, v70
	v_max_f32_e32 v69, v49, v49
	v_max_f32_e32 v70, v48, v48
	v_max_f32_e32 v69, v70, v69
	v_max_f32_e32 v70, v51, v51
	v_max_f32_e32 v71, v50, v50
	v_max_f32_e32 v70, v71, v70
	v_max3_f32 v68, v68, v69, v70
	v_max_f32_e32 v69, v53, v53
	v_max_f32_e32 v70, v52, v52
	s_waitcnt lgkmcnt(1)
	v_mfma_f32_16x16x32_bf16 v[64:67], v[208:211], v[88:91], v[64:67]
	v_max_f32_e32 v69, v70, v69
	v_max_f32_e32 v70, v55, v55
	v_max_f32_e32 v71, v54, v54
	v_max_f32_e32 v70, v71, v70
	v_max3_f32 v68, v68, v69, v70
	v_max_f32_e32 v69, v57, v57
	v_max_f32_e32 v70, v56, v56
	v_max_f32_e32 v69, v70, v69
	v_max_f32_e32 v70, v59, v59
	v_max_f32_e32 v71, v58, v58
	s_waitcnt lgkmcnt(0)
	v_mfma_f32_16x16x32_bf16 v[64:67], v[212:215], v[92:95], v[64:67]
	v_max_f32_e32 v70, v71, v70
	v_max3_f32 v68, v68, v69, v70
	v_max_f32_e32 v69, v61, v61
	v_max_f32_e32 v70, v60, v60
	v_max_f32_e32 v69, v70, v69
	v_max_f32_e32 v70, v63, v63
	v_max_f32_e32 v71, v62, v62
	v_max_f32_e32 v70, v71, v70
	v_max3_f32 v68, v68, v69, v70
	v_max_f32_e32 v69, v65, v65
	v_max_f32_e32 v70, v64, v64
	v_max_f32_e32 v69, v70, v69
	v_max_f32_e32 v70, v67, v67
	v_max_f32_e32 v71, v66, v66
	v_max_f32_e32 v70, v71, v70
	v_max3_f32 v68, v68, v69, v70
	ds_bpermute_b32 v69, v148, v68
	s_waitcnt lgkmcnt(0)
	v_max_f32_e32 v69, v69, v69
	v_max_f32_e32 v68, v68, v69
	ds_bpermute_b32 v69, v149, v68
	s_waitcnt lgkmcnt(0)
	v_max_f32_e32 v69, v69, v69
	v_max_f32_e32 v74, v68, v69
	v_sub_f32_e32 v4, v4, v74
	v_exp_f32_e32 v68, v4
	v_sub_f32_e32 v4, v12, v74
	v_exp_f32_e32 v69, v4
	v_sub_f32_e32 v4, v5, v74
	v_exp_f32_e32 v12, v4
	v_sub_f32_e32 v4, v13, v74
	v_exp_f32_e32 v13, v4
	v_sub_f32_e32 v4, v6, v74
	v_exp_f32_e32 v70, v4
	v_sub_f32_e32 v4, v14, v74
	v_exp_f32_e32 v71, v4
	v_sub_f32_e32 v4, v7, v74
	v_exp_f32_e32 v6, v4
	v_sub_f32_e32 v4, v15, v74
	v_exp_f32_e32 v7, v4
	v_pk_add_f32 v[4:5], v[68:69], v[12:13]
	v_sub_f32_e32 v9, v9, v74
	v_sub_f32_e32 v8, v8, v74
	v_pk_add_f32 v[14:15], v[70:71], v[6:7]
	v_exp_f32_e32 v8, v8
	v_pk_add_f32 v[72:73], v[4:5], v[14:15]
	v_exp_f32_e32 v14, v9
	v_sub_f32_e32 v9, v21, v74
	v_cvt_pk_bf16_f32 v4, v68, v12
	v_sub_f32_e32 v12, v20, v74
	v_exp_f32_e32 v20, v9
	v_sub_f32_e32 v9, v10, v74
	v_sub_f32_e32 v10, v22, v74
	v_cvt_pk_bf16_f32 v5, v70, v6
	v_cvt_pk_bf16_f32 v6, v69, v13
	v_exp_f32_e32 v13, v10
	v_sub_f32_e32 v10, v11, v74
	v_exp_f32_e32 v15, v10
	v_sub_f32_e32 v10, v23, v74
	v_exp_f32_e32 v12, v12
	v_exp_f32_e32 v21, v10
	v_exp_f32_e32 v9, v9
	v_cvt_pk_bf16_f32 v7, v71, v7
	v_cvt_pk_bf16_f32 v10, v12, v20
	v_pk_add_f32 v[68:69], v[12:13], v[20:21]
	v_cvt_pk_bf16_f32 v11, v13, v21
	v_sub_f32_e32 v13, v32, v74
	v_pk_add_f32 v[22:23], v[8:9], v[14:15]
	v_cvt_pk_bf16_f32 v8, v8, v14
	v_sub_f32_e32 v12, v16, v74
	v_exp_f32_e32 v14, v13
	v_sub_f32_e32 v13, v17, v74
	v_sub_f32_e32 v16, v18, v74
	v_sub_f32_e32 v18, v19, v74
	v_exp_f32_e32 v12, v12
	v_exp_f32_e32 v13, v13
	v_exp_f32_e32 v16, v16
	v_exp_f32_e32 v19, v18
	v_cvt_pk_bf16_f32 v9, v9, v15
	v_sub_f32_e32 v15, v33, v74
	v_sub_f32_e32 v17, v34, v74
	v_sub_f32_e32 v18, v35, v74
	v_exp_f32_e32 v15, v15
	v_exp_f32_e32 v17, v17
	v_exp_f32_e32 v21, v18
	v_add_f32_e32 v18, v12, v13
	v_add_f32_e32 v20, v16, v19
	v_cvt_pk_bf16_f32 v12, v12, v13
	v_cvt_pk_bf16_f32 v13, v16, v19
	v_sub_f32_e32 v16, v24, v74
	v_exp_f32_e32 v70, v16
	v_sub_f32_e32 v16, v36, v74
	v_exp_f32_e32 v19, v16
	v_sub_f32_e32 v16, v25, v74
	v_exp_f32_e32 v131, v16
	v_sub_f32_e32 v16, v37, v74
	v_add_f32_e32 v32, v14, v15
	v_add_f32_e32 v34, v17, v21
	v_cvt_pk_bf16_f32 v14, v14, v15
	v_cvt_pk_bf16_f32 v15, v17, v21
	v_exp_f32_e32 v21, v16
	v_sub_f32_e32 v16, v26, v74
	v_exp_f32_e32 v26, v16
	v_sub_f32_e32 v16, v38, v74
	v_exp_f32_e32 v33, v16
	v_sub_f32_e32 v16, v27, v74
	v_exp_f32_e32 v27, v16
	v_sub_f32_e32 v16, v39, v74
	v_exp_f32_e32 v35, v16
	v_pk_add_f32 v[16:17], v[72:73], v[72:73] op_sel:[0,1] op_sel_hi:[1,0]
	v_pk_add_f32 v[22:23], v[22:23], v[22:23] op_sel:[0,1] op_sel_hi:[1,0]
	v_pk_add_f32 v[24:25], v[68:69], v[68:69] op_sel:[0,1] op_sel_hi:[1,0]
	v_mov_b32_e32 v17, v70
	v_mov_b32_e32 v23, v26
	v_mov_b32_e32 v25, v27
	v_pk_add_f32 v[16:17], v[16:17], v[130:131]
	v_pk_add_f32 v[22:23], v[22:23], v[24:25]
	v_pk_add_f32 v[24:25], v[32:33], v[34:35]
	v_pk_add_f32 v[16:17], v[16:17], v[22:23]
	v_pk_add_f32 v[22:23], v[18:19], v[20:21]
	v_sub_f32_e32 v20, v28, v74
	v_pk_add_f32 v[22:23], v[22:23], v[24:25]
	v_cvt_pk_bf16_f32 v18, v19, v21
	v_pk_add_f32 v[36:37], v[16:17], v[22:23]
	v_exp_f32_e32 v22, v20
	v_sub_f32_e32 v20, v40, v74
	v_exp_f32_e32 v23, v20
	v_sub_f32_e32 v20, v29, v74
	v_exp_f32_e32 v24, v20
	v_sub_f32_e32 v20, v41, v74
	v_exp_f32_e32 v25, v20
	v_sub_f32_e32 v20, v30, v74
	v_cvt_pk_bf16_f32 v17, v26, v27
	v_exp_f32_e32 v26, v20
	v_sub_f32_e32 v20, v42, v74
	v_exp_f32_e32 v27, v20
	v_sub_f32_e32 v20, v31, v74
	v_exp_f32_e32 v28, v20
	v_sub_f32_e32 v20, v43, v74
	v_exp_f32_e32 v29, v20
	v_pk_add_f32 v[20:21], v[22:23], v[24:25]
	v_cvt_pk_bf16_f32 v19, v33, v35
	v_sub_f32_e32 v40, v54, v74
	v_pk_add_f32 v[30:31], v[26:27], v[28:29]
	v_exp_f32_e32 v41, v40
	v_pk_add_f32 v[32:33], v[20:21], v[30:31]
	v_cvt_pk_bf16_f32 v20, v22, v24
	v_cvt_pk_bf16_f32 v22, v23, v25
	v_sub_f32_e32 v25, v48, v74
	v_cvt_pk_bf16_f32 v21, v26, v28
	v_exp_f32_e32 v26, v25
	v_sub_f32_e32 v25, v45, v74
	v_exp_f32_e32 v28, v25
	v_sub_f32_e32 v25, v49, v74
	v_cvt_pk_bf16_f32 v23, v27, v29
	v_sub_f32_e32 v24, v44, v74
	v_exp_f32_e32 v30, v25
	v_sub_f32_e32 v25, v46, v74
	v_sub_f32_e32 v29, v47, v74
	v_exp_f32_e32 v24, v24
	v_exp_f32_e32 v25, v25
	v_sub_f32_e32 v27, v50, v74
	v_exp_f32_e32 v29, v29
	v_sub_f32_e32 v31, v51, v74
	v_exp_f32_e32 v27, v27
	v_exp_f32_e32 v31, v31
	v_sub_f32_e32 v40, v58, v74
	v_pk_add_f32 v[34:35], v[24:25], v[28:29]
	v_cvt_pk_bf16_f32 v25, v25, v29
	v_sub_f32_e32 v29, v56, v74
	v_exp_f32_e32 v43, v40
	v_sub_f32_e32 v40, v55, v74
	v_pk_add_f32 v[38:39], v[26:27], v[30:31]
	v_cvt_pk_bf16_f32 v24, v24, v28
	v_cvt_pk_bf16_f32 v26, v26, v30
	v_cvt_pk_bf16_f32 v27, v27, v31
	v_sub_f32_e32 v28, v52, v74
	v_exp_f32_e32 v30, v29
	v_sub_f32_e32 v29, v53, v74
	v_sub_f32_e32 v31, v57, v74
	v_exp_f32_e32 v45, v40
	v_sub_f32_e32 v40, v59, v74
	v_exp_f32_e32 v28, v28
	v_exp_f32_e32 v29, v29
	v_exp_f32_e32 v31, v31
	v_exp_f32_e32 v47, v40
	v_add_f32_e32 v42, v41, v45
	v_add_f32_e32 v40, v28, v29
	v_add_f32_e32 v44, v30, v31
	v_add_f32_e32 v46, v43, v47
	v_cvt_pk_bf16_f32 v28, v28, v29
	v_cvt_pk_bf16_f32 v29, v41, v45
	v_cvt_pk_bf16_f32 v30, v30, v31
	v_cvt_pk_bf16_f32 v31, v43, v47
	v_sub_f32_e32 v41, v60, v74
	v_sub_f32_e32 v43, v61, v74
	v_exp_f32_e32 v48, v41
	v_exp_f32_e32 v49, v43
	v_sub_f32_e32 v45, v62, v74
	v_sub_f32_e32 v47, v63, v74
	v_exp_f32_e32 v50, v45
	v_exp_f32_e32 v51, v47
	v_sub_f32_e32 v41, v64, v74
	v_sub_f32_e32 v43, v65, v74
	v_sub_f32_e32 v45, v66, v74
	v_sub_f32_e32 v47, v67, v74
	v_pk_add_f32 v[36:37], v[36:37], v[36:37] op_sel:[0,1] op_sel_hi:[1,0]
	v_pk_add_f32 v[32:33], v[32:33], v[32:33] op_sel:[0,1] op_sel_hi:[1,0]
	v_exp_f32_e32 v41, v41
	v_exp_f32_e32 v43, v43
	v_exp_f32_e32 v45, v45
	v_exp_f32_e32 v47, v47
	v_mov_b32_e32 v37, v48
	v_mov_b32_e32 v33, v49
	v_pk_add_f32 v[32:33], v[36:37], v[32:33]
	v_pk_add_f32 v[34:35], v[34:35], v[34:35] op_sel:[0,1] op_sel_hi:[1,0]
	v_pk_add_f32 v[36:37], v[38:39], v[38:39] op_sel:[0,1] op_sel_hi:[1,0]
	v_mov_b32_e32 v35, v50
	v_mov_b32_e32 v37, v51
	v_pk_add_f32 v[34:35], v[34:35], v[36:37]
	v_pk_add_f32 v[36:37], v[44:45], v[46:47]
	v_pk_add_f32 v[32:33], v[32:33], v[34:35]
	v_pk_add_f32 v[34:35], v[40:41], v[42:43]
	v_cvt_pk_bf16_f32 v16, v70, v131
	v_pk_add_f32 v[34:35], v[34:35], v[36:37]
	s_nop 0
	v_pk_add_f32 v[32:33], v[32:33], v[34:35]
	v_cvt_pk_bf16_f32 v34, v41, v43
	v_add_f32_e32 v36, v32, v33
	ds_bpermute_b32 v37, v148, v36
	v_cvt_pk_bf16_f32 v32, v48, v49
	v_cvt_pk_bf16_f32 v33, v50, v51
	v_cvt_pk_bf16_f32 v35, v45, v47
	s_waitcnt lgkmcnt(0)
	v_add_f32_e32 v36, v36, v37
	ds_bpermute_b32 v37, v149, v36
	s_waitcnt lgkmcnt(0)
	v_add_f32_e32 v36, v36, v37
	v_rcp_f32_e32 v136, v36
	v_mov_b32_e32 v36, 16
	s_nop 0
	v_ashrrev_i32_e32 v37, 31, v36
	v_lshl_add_u64 v[36:37], v[96:97], 0, v[36:37]
	v_lshlrev_b64 v[36:37], 11, v[36:37]
	v_lshl_add_u64 v[36:37], v[98:99], 0, v[36:37]
	global_load_dwordx4 v[68:71], v[36:37], off
	global_load_dwordx4 v[72:75], v[36:37], off offset:64
	global_load_dwordx4 v[76:79], v[36:37], off offset:128
	global_load_dwordx4 v[80:83], v[36:37], off offset:192
	global_load_dwordx4 v[84:87], v[36:37], off offset:256
	global_load_dwordx4 v[88:91], v[36:37], off offset:320
	global_load_dwordx4 v[92:95], v[36:37], off offset:384
	global_load_dwordx4 v[96:99], v[36:37], off offset:448
	ds_read_b128 v[160:163], v188
	ds_read_b128 v[164:167], v187
	ds_read_b128 v[168:171], v186
	ds_read_b128 v[172:175], v137
	ds_read_b128 v[192:195], v188 offset:256
	ds_read_b128 v[200:203], v187 offset:256
	ds_read_b128 v[204:207], v186 offset:256
	ds_read_b128 v[208:211], v137 offset:256
	s_waitcnt vmcnt(7)
	s_waitcnt lgkmcnt(7)
	v_mfma_f32_16x16x32_bf16 v[64:67], v[160:163], v[68:71], 0
	ds_read_b128 v[212:215], v188 offset:8192
	s_waitcnt vmcnt(6)
	s_waitcnt lgkmcnt(7)
	v_mfma_f32_16x16x32_bf16 v[60:63], v[164:167], v[72:75], v[64:67]
	ds_read_b128 v[252:255], v187 offset:8192
	s_waitcnt vmcnt(5)
	s_waitcnt lgkmcnt(7)
	v_mfma_f32_16x16x32_bf16 v[56:59], v[168:171], v[76:79], v[60:63]
	ds_read_b128 v[160:163], v186 offset:8192
	s_waitcnt vmcnt(4)
	s_waitcnt lgkmcnt(7)
	v_mfma_f32_16x16x32_bf16 v[52:55], v[172:175], v[80:83], v[56:59]
	ds_read_b128 v[164:167], v137 offset:8192
	s_waitcnt vmcnt(3)
	s_waitcnt lgkmcnt(7)
	v_mfma_f32_16x16x32_bf16 v[48:51], v[192:195], v[84:87], v[52:55]
	ds_read_b128 v[168:171], v188 offset:8448
	s_waitcnt vmcnt(2)
	s_waitcnt lgkmcnt(7)
	v_mfma_f32_16x16x32_bf16 v[44:47], v[200:203], v[88:91], v[48:51]
	ds_read_b128 v[172:175], v187 offset:8448
	s_waitcnt vmcnt(1)
	s_waitcnt lgkmcnt(7)
	v_mfma_f32_16x16x32_bf16 v[40:43], v[204:207], v[92:95], v[44:47]
	ds_read_b128 v[192:195], v186 offset:8448
	s_waitcnt vmcnt(0)
	s_waitcnt lgkmcnt(7)
	v_mfma_f32_16x16x32_bf16 v[44:47], v[208:211], v[96:99], v[40:43]
	ds_read_b128 v[200:203], v137 offset:8448
	s_nop 4
	s_waitcnt lgkmcnt(7)
	v_mfma_f32_16x16x32_bf16 v[222:225], v[212:215], v[68:71], 0
	ds_read_b128 v[204:207], v188 offset:16384
	s_waitcnt lgkmcnt(7)
	v_mfma_f32_16x16x32_bf16 v[64:67], v[252:255], v[72:75], v[222:225]
	ds_read_b128 v[208:211], v187 offset:16384
	s_waitcnt lgkmcnt(7)
	v_mfma_f32_16x16x32_bf16 v[60:63], v[160:163], v[76:79], v[64:67]
	ds_read_b128 v[212:215], v186 offset:16384
	s_waitcnt lgkmcnt(7)
	v_mfma_f32_16x16x32_bf16 v[56:59], v[164:167], v[80:83], v[60:63]
	ds_read_b128 v[252:255], v137 offset:16384
	s_waitcnt lgkmcnt(7)
	v_mfma_f32_16x16x32_bf16 v[52:55], v[168:171], v[84:87], v[56:59]
	ds_read_b128 v[160:163], v188 offset:16640
	s_waitcnt lgkmcnt(7)
	v_mfma_f32_16x16x32_bf16 v[48:51], v[172:175], v[88:91], v[52:55]
	ds_read_b128 v[164:167], v187 offset:16640
	s_waitcnt lgkmcnt(7)
	v_mfma_f32_16x16x32_bf16 v[40:43], v[192:195], v[92:95], v[48:51]
	ds_read_b128 v[168:171], v186 offset:16640
	s_waitcnt lgkmcnt(7)
	v_mfma_f32_16x16x32_bf16 v[60:63], v[200:203], v[96:99], v[40:43]
	ds_read_b128 v[172:175], v137 offset:16640
	s_nop 5
	s_waitcnt lgkmcnt(7)
	v_mfma_f32_16x16x32_bf16 v[226:229], v[204:207], v[68:71], 0
	ds_read_b128 v[192:195], v188 offset:24576
	s_waitcnt lgkmcnt(7)
	v_mfma_f32_16x16x32_bf16 v[222:225], v[208:211], v[72:75], v[226:229]
	ds_read_b128 v[200:203], v187 offset:24576
	s_waitcnt lgkmcnt(7)
	v_mfma_f32_16x16x32_bf16 v[64:67], v[212:215], v[76:79], v[222:225]
	ds_read_b128 v[204:207], v186 offset:24576
	s_waitcnt lgkmcnt(7)
	v_mfma_f32_16x16x32_bf16 v[56:59], v[252:255], v[80:83], v[64:67]
	ds_read_b128 v[208:211], v137 offset:24576
	s_waitcnt lgkmcnt(7)
	v_mfma_f32_16x16x32_bf16 v[52:55], v[160:163], v[84:87], v[56:59]
	ds_read_b128 v[212:215], v188 offset:24832
	s_waitcnt lgkmcnt(7)
	v_mfma_f32_16x16x32_bf16 v[48:51], v[164:167], v[88:91], v[52:55]
	ds_read_b128 v[252:255], v187 offset:24832
	s_waitcnt lgkmcnt(7)
	v_mfma_f32_16x16x32_bf16 v[40:43], v[168:171], v[92:95], v[48:51]
	ds_read_b128 v[160:163], v186 offset:24832
	s_waitcnt lgkmcnt(7)
	v_mfma_f32_16x16x32_bf16 v[36:39], v[172:175], v[96:99], v[40:43]
	ds_read_b128 v[164:167], v137 offset:24832
	s_nop 6
	s_waitcnt lgkmcnt(7)
	v_mfma_f32_16x16x32_bf16 v[230:233], v[192:195], v[68:71], 0
	ds_read_b128 v[168:171], v188 offset:32768
	s_waitcnt lgkmcnt(7)
	v_mfma_f32_16x16x32_bf16 v[226:229], v[200:203], v[72:75], v[230:233]
	ds_read_b128 v[172:175], v187 offset:32768
	s_waitcnt lgkmcnt(7)
	v_mfma_f32_16x16x32_bf16 v[222:225], v[204:207], v[76:79], v[226:229]
	ds_read_b128 v[192:195], v186 offset:32768
	s_waitcnt lgkmcnt(7)
	v_mfma_f32_16x16x32_bf16 v[64:67], v[208:211], v[80:83], v[222:225]
	ds_read_b128 v[200:203], v137 offset:32768
	s_waitcnt lgkmcnt(7)
	v_mfma_f32_16x16x32_bf16 v[56:59], v[212:215], v[84:87], v[64:67]
	ds_read_b128 v[204:207], v188 offset:33024
	s_waitcnt lgkmcnt(7)
	v_mfma_f32_16x16x32_bf16 v[52:55], v[252:255], v[88:91], v[56:59]
	ds_read_b128 v[208:211], v187 offset:33024
	s_waitcnt lgkmcnt(7)
	v_mfma_f32_16x16x32_bf16 v[48:51], v[160:163], v[92:95], v[52:55]
	ds_read_b128 v[212:215], v186 offset:33024
	s_waitcnt lgkmcnt(7)
	v_mfma_f32_16x16x32_bf16 v[52:55], v[164:167], v[96:99], v[48:51]
	ds_read_b128 v[252:255], v137 offset:33024
	s_nop 5
	s_waitcnt lgkmcnt(7)
	v_mfma_f32_16x16x32_bf16 v[234:237], v[168:171], v[68:71], 0
	ds_read_b128 v[160:163], v188 offset:40960
	s_waitcnt lgkmcnt(7)
	v_mfma_f32_16x16x32_bf16 v[230:233], v[172:175], v[72:75], v[234:237]
	ds_read_b128 v[164:167], v187 offset:40960
	s_waitcnt lgkmcnt(7)
	v_mfma_f32_16x16x32_bf16 v[226:229], v[192:195], v[76:79], v[230:233]
	ds_read_b128 v[168:171], v186 offset:40960
	s_waitcnt lgkmcnt(7)
	v_mfma_f32_16x16x32_bf16 v[222:225], v[200:203], v[80:83], v[226:229]
	ds_read_b128 v[172:175], v137 offset:40960
	s_waitcnt lgkmcnt(7)
	v_mfma_f32_16x16x32_bf16 v[64:67], v[204:207], v[84:87], v[222:225]
	ds_read_b128 v[192:195], v188 offset:41216
	s_waitcnt lgkmcnt(7)
	v_mfma_f32_16x16x32_bf16 v[56:59], v[208:211], v[88:91], v[64:67]
	ds_read_b128 v[200:203], v187 offset:41216
	s_waitcnt lgkmcnt(7)
	v_mfma_f32_16x16x32_bf16 v[48:51], v[212:215], v[92:95], v[56:59]
	ds_read_b128 v[204:207], v186 offset:41216
	s_waitcnt lgkmcnt(7)
	v_mfma_f32_16x16x32_bf16 v[40:43], v[252:255], v[96:99], v[48:51]
	ds_read_b128 v[208:211], v137 offset:41216
	s_nop 6
	s_waitcnt lgkmcnt(7)
	v_mfma_f32_16x16x32_bf16 v[238:241], v[160:163], v[68:71], 0
	ds_read_b128 v[212:215], v188 offset:49152
	s_waitcnt lgkmcnt(7)
	v_mfma_f32_16x16x32_bf16 v[234:237], v[164:167], v[72:75], v[238:241]
	ds_read_b128 v[252:255], v187 offset:49152
	s_waitcnt lgkmcnt(7)
	v_mfma_f32_16x16x32_bf16 v[230:233], v[168:171], v[76:79], v[234:237]
	ds_read_b128 v[160:163], v186 offset:49152
	s_waitcnt lgkmcnt(7)
	v_mfma_f32_16x16x32_bf16 v[226:229], v[172:175], v[80:83], v[230:233]
	ds_read_b128 v[164:167], v137 offset:49152
	s_waitcnt lgkmcnt(7)
	v_mfma_f32_16x16x32_bf16 v[222:225], v[192:195], v[84:87], v[226:229]
	ds_read_b128 v[168:171], v188 offset:49408
	s_waitcnt lgkmcnt(7)
	v_mfma_f32_16x16x32_bf16 v[64:67], v[200:203], v[88:91], v[222:225]
	ds_read_b128 v[172:175], v187 offset:49408
	s_waitcnt lgkmcnt(7)
	v_mfma_f32_16x16x32_bf16 v[56:59], v[204:207], v[92:95], v[64:67]
	ds_read_b128 v[192:195], v186 offset:49408
	s_waitcnt lgkmcnt(7)
	v_mfma_f32_16x16x32_bf16 v[56:59], v[208:211], v[96:99], v[56:59]
	ds_read_b128 v[200:203], v137 offset:49408
	s_nop 4
	s_waitcnt lgkmcnt(7)
	v_mfma_f32_16x16x32_bf16 v[242:245], v[212:215], v[68:71], 0
	ds_read_b128 v[204:207], v188 offset:57344
	s_waitcnt lgkmcnt(7)
	v_mfma_f32_16x16x32_bf16 v[238:241], v[252:255], v[72:75], v[242:245]
	ds_read_b128 v[208:211], v187 offset:57344
	s_waitcnt lgkmcnt(7)
	v_mfma_f32_16x16x32_bf16 v[234:237], v[160:163], v[76:79], v[238:241]
	ds_read_b128 v[212:215], v186 offset:57344
	s_waitcnt lgkmcnt(7)
	v_mfma_f32_16x16x32_bf16 v[230:233], v[164:167], v[80:83], v[234:237]
	ds_read_b128 v[252:255], v137 offset:57344
	s_waitcnt lgkmcnt(7)
	v_mfma_f32_16x16x32_bf16 v[226:229], v[168:171], v[84:87], v[230:233]
	ds_read_b128 v[160:163], v188 offset:57600
	s_waitcnt lgkmcnt(7)
	v_mfma_f32_16x16x32_bf16 v[222:225], v[172:175], v[88:91], v[226:229]
	ds_read_b128 v[164:167], v187 offset:57600
	s_waitcnt lgkmcnt(7)
	v_mfma_f32_16x16x32_bf16 v[64:67], v[192:195], v[92:95], v[222:225]
	ds_read_b128 v[168:171], v186 offset:57600
	s_waitcnt lgkmcnt(7)
	v_mfma_f32_16x16x32_bf16 v[48:51], v[200:203], v[96:99], v[64:67]
	ds_read_b128 v[172:175], v137 offset:57600
	s_nop 6
	s_waitcnt lgkmcnt(0)
	s_barrier
	s_waitcnt lgkmcnt(7)
	v_mfma_f32_16x16x32_bf16 v[246:249], v[204:207], v[68:71], 0
	ds_read_b128 v[192:195], v135
	buffer_load_dwordx4 v140, s[8:11], 0 offen lds
	s_mov_b32 m0, s30
	s_waitcnt lgkmcnt(7)
	v_mfma_f32_16x16x32_bf16 v[242:245], v[208:211], v[72:75], v[246:249]
	ds_read_b128 v[200:203], v159
	buffer_load_dwordx4 v141, s[8:11], 0 offen lds
	s_mov_b32 m0, s31
	s_waitcnt lgkmcnt(7)
	v_mfma_f32_16x16x32_bf16 v[238:241], v[212:215], v[76:79], v[242:245]
	ds_read_b128 v[204:207], v176
	buffer_load_dwordx4 v142, s[8:11], 0 offen lds
	s_mov_b32 m0, s35
	s_waitcnt lgkmcnt(7)
	v_mfma_f32_16x16x32_bf16 v[234:237], v[252:255], v[80:83], v[238:241]
	ds_read_b128 v[208:211], v177
	buffer_load_dwordx4 v143, s[8:11], 0 offen lds
	s_mov_b32 m0, s37
	s_waitcnt lgkmcnt(7)
	v_mfma_f32_16x16x32_bf16 v[230:233], v[160:163], v[84:87], v[234:237]
	ds_read_b128 v[212:215], v135 offset:256
	buffer_load_dwordx4 v144, s[8:11], 0 offen lds
	s_mov_b32 m0, s39
	s_waitcnt lgkmcnt(7)
	v_mfma_f32_16x16x32_bf16 v[226:229], v[164:167], v[88:91], v[230:233]
	ds_read_b128 v[252:255], v159 offset:256
	buffer_load_dwordx4 v145, s[8:11], 0 offen lds
	s_mov_b32 m0, s41
	s_waitcnt lgkmcnt(7)
	v_mfma_f32_16x16x32_bf16 v[222:225], v[168:171], v[92:95], v[226:229]
	ds_read_b128 v[160:163], v176 offset:256
	buffer_load_dwordx4 v146, s[8:11], 0 offen lds
	s_mov_b32 m0, s48
	s_nop 0
	buffer_load_dwordx4 v147, s[8:11], 0 offen lds
	s_waitcnt lgkmcnt(7)
	v_mfma_f32_16x16x32_bf16 v[64:67], v[172:175], v[96:99], v[222:225]
	ds_read_b128 v[164:167], v177 offset:256
	s_mov_b32 m0, s50
	s_nop 0
	s_waitcnt lgkmcnt(7)
	v_mfma_f32_16x16x32_bf16 v[222:225], v[192:195], v[68:71], 0
	ds_read_b128 v[168:171], v135 offset:8192
	s_waitcnt lgkmcnt(7)
	v_mfma_f32_16x16x32_bf16 v[222:225], v[200:203], v[72:75], v[222:225]
	ds_read_b128 v[172:175], v159 offset:8192
	s_waitcnt lgkmcnt(7)
	v_mfma_f32_16x16x32_bf16 v[222:225], v[204:207], v[76:79], v[222:225]
	ds_read_b128 v[192:195], v176 offset:8192
	s_waitcnt lgkmcnt(7)
	v_mfma_f32_16x16x32_bf16 v[222:225], v[208:211], v[80:83], v[222:225]
	ds_read_b128 v[200:203], v177 offset:8192
	s_waitcnt lgkmcnt(7)
	v_mfma_f32_16x16x32_bf16 v[222:225], v[212:215], v[84:87], v[222:225]
	ds_read_b128 v[204:207], v135 offset:8448
	s_waitcnt lgkmcnt(7)
	v_mfma_f32_16x16x32_bf16 v[222:225], v[252:255], v[88:91], v[222:225]
	ds_read_b128 v[208:211], v159 offset:8448
	s_waitcnt lgkmcnt(7)
	v_mfma_f32_16x16x32_bf16 v[222:225], v[160:163], v[92:95], v[222:225]
	ds_read_b128 v[212:215], v176 offset:8448
	s_waitcnt lgkmcnt(7)
	v_mfma_f32_16x16x32_bf16 v[100:103], v[164:167], v[96:99], v[222:225]
	ds_read_b128 v[252:255], v177 offset:8448
	s_nop 5
	s_waitcnt lgkmcnt(7)
	v_mfma_f32_16x16x32_bf16 v[104:107], v[168:171], v[68:71], 0
	ds_read_b128 v[160:163], v135 offset:16384
	s_waitcnt lgkmcnt(7)
	v_mfma_f32_16x16x32_bf16 v[104:107], v[172:175], v[72:75], v[104:107]
	ds_read_b128 v[164:167], v159 offset:16384
	s_waitcnt lgkmcnt(7)
	v_mfma_f32_16x16x32_bf16 v[104:107], v[192:195], v[76:79], v[104:107]
	ds_read_b128 v[168:171], v176 offset:16384
	s_waitcnt lgkmcnt(7)
	v_mfma_f32_16x16x32_bf16 v[104:107], v[200:203], v[80:83], v[104:107]
	ds_read_b128 v[172:175], v177 offset:16384
	s_waitcnt lgkmcnt(7)
	v_mfma_f32_16x16x32_bf16 v[104:107], v[204:207], v[84:87], v[104:107]
	ds_read_b128 v[192:195], v135 offset:16640
	s_waitcnt lgkmcnt(7)
	v_mfma_f32_16x16x32_bf16 v[104:107], v[208:211], v[88:91], v[104:107]
	ds_read_b128 v[200:203], v159 offset:16640
	s_waitcnt lgkmcnt(7)
	v_mfma_f32_16x16x32_bf16 v[104:107], v[212:215], v[92:95], v[104:107]
	ds_read_b128 v[204:207], v176 offset:16640
	s_waitcnt lgkmcnt(7)
	v_mfma_f32_16x16x32_bf16 v[104:107], v[252:255], v[96:99], v[104:107]
	ds_read_b128 v[208:211], v177 offset:16640
	s_waitcnt lgkmcnt(7)
	v_mfma_f32_16x16x32_bf16 v[108:111], v[160:163], v[68:71], 0
	ds_read_b128 v[212:215], v135 offset:24576
	s_waitcnt lgkmcnt(7)
	v_mfma_f32_16x16x32_bf16 v[108:111], v[164:167], v[72:75], v[108:111]
	ds_read_b128 v[252:255], v159 offset:24576
	s_waitcnt lgkmcnt(7)
	v_mfma_f32_16x16x32_bf16 v[108:111], v[168:171], v[76:79], v[108:111]
	ds_read_b128 v[160:163], v176 offset:24576
	s_waitcnt lgkmcnt(7)
	v_mfma_f32_16x16x32_bf16 v[108:111], v[172:175], v[80:83], v[108:111]
	ds_read_b128 v[164:167], v177 offset:24576
	s_waitcnt lgkmcnt(7)
	v_mfma_f32_16x16x32_bf16 v[108:111], v[192:195], v[84:87], v[108:111]
	ds_read_b128 v[168:171], v135 offset:24832
	s_waitcnt lgkmcnt(7)
	v_mfma_f32_16x16x32_bf16 v[108:111], v[200:203], v[88:91], v[108:111]
	ds_read_b128 v[172:175], v159 offset:24832
	s_waitcnt lgkmcnt(7)
	v_mfma_f32_16x16x32_bf16 v[108:111], v[204:207], v[92:95], v[108:111]
	ds_read_b128 v[192:195], v176 offset:24832
	s_waitcnt lgkmcnt(7)
	v_mfma_f32_16x16x32_bf16 v[108:111], v[208:211], v[96:99], v[108:111]
	ds_read_b128 v[200:203], v177 offset:24832
	s_waitcnt lgkmcnt(7)
	v_mfma_f32_16x16x32_bf16 v[112:115], v[212:215], v[68:71], 0
	ds_read_b128 v[204:207], v135 offset:32768
	s_waitcnt lgkmcnt(7)
	v_mfma_f32_16x16x32_bf16 v[112:115], v[252:255], v[72:75], v[112:115]
	ds_read_b128 v[208:211], v159 offset:32768
	s_waitcnt lgkmcnt(7)
	v_mfma_f32_16x16x32_bf16 v[112:115], v[160:163], v[76:79], v[112:115]
	ds_read_b128 v[212:215], v176 offset:32768
	s_waitcnt lgkmcnt(7)
	v_mfma_f32_16x16x32_bf16 v[112:115], v[164:167], v[80:83], v[112:115]
	ds_read_b128 v[252:255], v177 offset:32768
	s_waitcnt lgkmcnt(7)
	v_mfma_f32_16x16x32_bf16 v[112:115], v[168:171], v[84:87], v[112:115]
	ds_read_b128 v[160:163], v135 offset:33024
	s_waitcnt lgkmcnt(7)
	v_mfma_f32_16x16x32_bf16 v[112:115], v[172:175], v[88:91], v[112:115]
	ds_read_b128 v[164:167], v159 offset:33024
	s_waitcnt lgkmcnt(7)
	v_mfma_f32_16x16x32_bf16 v[112:115], v[192:195], v[92:95], v[112:115]
	ds_read_b128 v[168:171], v176 offset:33024
	s_waitcnt lgkmcnt(7)
	v_mfma_f32_16x16x32_bf16 v[112:115], v[200:203], v[96:99], v[112:115]
	ds_read_b128 v[172:175], v177 offset:33024
	s_waitcnt lgkmcnt(7)
	v_mfma_f32_16x16x32_bf16 v[116:119], v[204:207], v[68:71], 0
	ds_read_b128 v[192:195], v135 offset:40960
	s_waitcnt lgkmcnt(7)
	v_mfma_f32_16x16x32_bf16 v[116:119], v[208:211], v[72:75], v[116:119]
	ds_read_b128 v[200:203], v159 offset:40960
	s_waitcnt lgkmcnt(7)
	v_mfma_f32_16x16x32_bf16 v[116:119], v[212:215], v[76:79], v[116:119]
	ds_read_b128 v[204:207], v176 offset:40960
	s_waitcnt lgkmcnt(7)
	v_mfma_f32_16x16x32_bf16 v[116:119], v[252:255], v[80:83], v[116:119]
	ds_read_b128 v[208:211], v177 offset:40960
	s_waitcnt lgkmcnt(7)
	v_mfma_f32_16x16x32_bf16 v[116:119], v[160:163], v[84:87], v[116:119]
	ds_read_b128 v[212:215], v135 offset:41216
	s_waitcnt lgkmcnt(7)
	v_mfma_f32_16x16x32_bf16 v[116:119], v[164:167], v[88:91], v[116:119]
	ds_read_b128 v[252:255], v159 offset:41216
	s_waitcnt lgkmcnt(7)
	v_mfma_f32_16x16x32_bf16 v[116:119], v[168:171], v[92:95], v[116:119]
	ds_read_b128 v[160:163], v176 offset:41216
	s_waitcnt lgkmcnt(7)
	v_mfma_f32_16x16x32_bf16 v[116:119], v[172:175], v[96:99], v[116:119]
	ds_read_b128 v[164:167], v177 offset:41216
	s_waitcnt lgkmcnt(7)
	v_mfma_f32_16x16x32_bf16 v[120:123], v[192:195], v[68:71], 0
	ds_read_b128 v[168:171], v135 offset:49152
	s_waitcnt lgkmcnt(7)
	v_mfma_f32_16x16x32_bf16 v[120:123], v[200:203], v[72:75], v[120:123]
	ds_read_b128 v[172:175], v159 offset:49152
	s_waitcnt lgkmcnt(7)
	v_mfma_f32_16x16x32_bf16 v[120:123], v[204:207], v[76:79], v[120:123]
	ds_read_b128 v[192:195], v176 offset:49152
	s_waitcnt lgkmcnt(7)
	v_mfma_f32_16x16x32_bf16 v[120:123], v[208:211], v[80:83], v[120:123]
	ds_read_b128 v[200:203], v177 offset:49152
	s_waitcnt lgkmcnt(7)
	v_mfma_f32_16x16x32_bf16 v[120:123], v[212:215], v[84:87], v[120:123]
	ds_read_b128 v[204:207], v135 offset:49408
	s_waitcnt lgkmcnt(7)
	v_mfma_f32_16x16x32_bf16 v[120:123], v[252:255], v[88:91], v[120:123]
	ds_read_b128 v[208:211], v159 offset:49408
	s_waitcnt lgkmcnt(7)
	v_mfma_f32_16x16x32_bf16 v[120:123], v[160:163], v[92:95], v[120:123]
	ds_read_b128 v[212:215], v176 offset:49408
	s_waitcnt lgkmcnt(7)
	v_mfma_f32_16x16x32_bf16 v[120:123], v[164:167], v[96:99], v[120:123]
	ds_read_b128 v[252:255], v177 offset:49408
	s_waitcnt lgkmcnt(7)
	v_mfma_f32_16x16x32_bf16 v[196:199], v[168:171], v[68:71], 0
	ds_read_b128 v[160:163], v135 offset:57344
	s_waitcnt lgkmcnt(7)
	v_mfma_f32_16x16x32_bf16 v[196:199], v[172:175], v[72:75], v[196:199]
	ds_read_b128 v[164:167], v159 offset:57344
	s_waitcnt lgkmcnt(7)
	v_mfma_f32_16x16x32_bf16 v[196:199], v[192:195], v[76:79], v[196:199]
	ds_read_b128 v[168:171], v176 offset:57344
	s_waitcnt lgkmcnt(7)
	v_mfma_f32_16x16x32_bf16 v[196:199], v[200:203], v[80:83], v[196:199]
	ds_read_b128 v[172:175], v177 offset:57344
	s_waitcnt lgkmcnt(7)
	v_mfma_f32_16x16x32_bf16 v[124:127], v[204:207], v[84:87], v[196:199]
	ds_read_b128 v[192:195], v135 offset:57600
	s_waitcnt lgkmcnt(7)
	v_mfma_f32_16x16x32_bf16 v[124:127], v[208:211], v[88:91], v[124:127]
	ds_read_b128 v[200:203], v159 offset:57600
	s_waitcnt lgkmcnt(7)
	v_mfma_f32_16x16x32_bf16 v[124:127], v[212:215], v[92:95], v[124:127]
	ds_read_b128 v[204:207], v176 offset:57600
	s_waitcnt lgkmcnt(7)
	v_mfma_f32_16x16x32_bf16 v[124:127], v[252:255], v[96:99], v[124:127]
	ds_read_b128 v[208:211], v177 offset:57600
	s_nop 3
	s_waitcnt vmcnt(0)
	s_waitcnt lgkmcnt(7)
	v_mfma_f32_16x16x32_bf16 v[68:71], v[160:163], v[68:71], 0
	s_waitcnt lgkmcnt(0)
	s_barrier
	buffer_load_dwordx4 v140, s[8:11], s49 offen lds
	s_waitcnt lgkmcnt(6)
	v_mfma_f32_16x16x32_bf16 v[68:71], v[164:167], v[72:75], v[68:71]
	v_max_f32_e32 v72, v45, v45
	v_max_f32_e32 v73, v44, v44
	v_max_f32_e32 v72, v73, v72
	v_max_f32_e32 v73, v47, v47
	v_max_f32_e32 v74, v46, v46
	v_max_f32_e32 v73, v74, v73
	v_max3_f32 v72, v72, s61, v73
	v_max_f32_e32 v73, v61, v61
	v_max_f32_e32 v74, v60, v60
	v_max_f32_e32 v73, v74, v73
	v_max_f32_e32 v74, v63, v63
	v_max_f32_e32 v75, v62, v62
	v_max_f32_e32 v74, v75, v74
	v_max3_f32 v72, v72, v73, v74
	v_max_f32_e32 v73, v37, v37
	v_max_f32_e32 v74, v36, v36
	v_max_f32_e32 v73, v74, v73
	v_max_f32_e32 v74, v39, v39
	v_max_f32_e32 v75, v38, v38
	v_max_f32_e32 v74, v75, v74
	v_max3_f32 v72, v72, v73, v74
	v_max_f32_e32 v73, v53, v53
	v_max_f32_e32 v74, v52, v52
	v_max_f32_e32 v73, v74, v73
	v_max_f32_e32 v74, v55, v55
	v_max_f32_e32 v75, v54, v54
	v_max_f32_e32 v74, v75, v74
	v_max3_f32 v72, v72, v73, v74
	v_max_f32_e32 v73, v41, v41
	v_max_f32_e32 v74, v40, v40
	v_max_f32_e32 v73, v74, v73
	v_max_f32_e32 v74, v43, v43
	v_max_f32_e32 v75, v42, v42
	v_max_f32_e32 v74, v75, v74
	v_max3_f32 v72, v72, v73, v74
	v_max_f32_e32 v73, v57, v57
	v_max_f32_e32 v74, v56, v56
	v_max_f32_e32 v73, v74, v73
	v_max_f32_e32 v74, v59, v59
	v_max_f32_e32 v75, v58, v58
	v_max_f32_e32 v74, v75, v74
	v_max3_f32 v72, v72, v73, v74
	v_max_f32_e32 v73, v49, v49
	v_max_f32_e32 v74, v48, v48
	v_max_f32_e32 v73, v74, v73
	v_max_f32_e32 v74, v51, v51
	v_max_f32_e32 v75, v50, v50
	v_max_f32_e32 v74, v75, v74
	s_waitcnt lgkmcnt(5)
	v_mfma_f32_16x16x32_bf16 v[68:71], v[168:171], v[76:79], v[68:71]
	v_max3_f32 v72, v72, v73, v74
	v_max_f32_e32 v73, v65, v65
	v_max_f32_e32 v74, v64, v64
	v_max_f32_e32 v73, v74, v73
	v_max_f32_e32 v74, v67, v67
	v_max_f32_e32 v75, v66, v66
	v_max_f32_e32 v74, v75, v74
	v_max3_f32 v72, v72, v73, v74
	v_max_f32_e32 v73, v101, v101
	v_max_f32_e32 v74, v100, v100
	s_waitcnt lgkmcnt(4)
	v_mfma_f32_16x16x32_bf16 v[68:71], v[172:175], v[80:83], v[68:71]
	v_max_f32_e32 v73, v74, v73
	v_max_f32_e32 v74, v103, v103
	v_max_f32_e32 v75, v102, v102
	v_max_f32_e32 v74, v75, v74
	v_max3_f32 v72, v72, v73, v74
	v_max_f32_e32 v73, v105, v105
	v_max_f32_e32 v74, v104, v104
	v_max_f32_e32 v73, v74, v73
	v_max_f32_e32 v74, v107, v107
	v_max_f32_e32 v75, v106, v106
	s_waitcnt lgkmcnt(3)
	v_mfma_f32_16x16x32_bf16 v[68:71], v[192:195], v[84:87], v[68:71]
	v_max_f32_e32 v74, v75, v74
	v_max3_f32 v72, v72, v73, v74
	v_max_f32_e32 v73, v109, v109
	v_max_f32_e32 v74, v108, v108
	v_max_f32_e32 v73, v74, v73
	v_max_f32_e32 v74, v111, v111
	v_max_f32_e32 v75, v110, v110
	v_max_f32_e32 v74, v75, v74
	s_waitcnt lgkmcnt(2)
	v_mfma_f32_16x16x32_bf16 v[68:71], v[200:203], v[88:91], v[68:71]
	v_max3_f32 v72, v72, v73, v74
	v_max_f32_e32 v73, v113, v113
	v_max_f32_e32 v74, v112, v112
	v_max_f32_e32 v73, v74, v73
	v_max_f32_e32 v74, v115, v115
	v_max_f32_e32 v75, v114, v114
	v_max_f32_e32 v74, v75, v74
	v_max3_f32 v72, v72, v73, v74
	v_max_f32_e32 v73, v117, v117
	v_max_f32_e32 v74, v116, v116
	s_waitcnt lgkmcnt(1)
	v_mfma_f32_16x16x32_bf16 v[68:71], v[204:207], v[92:95], v[68:71]
	v_max_f32_e32 v73, v74, v73
	v_max_f32_e32 v74, v119, v119
	v_max_f32_e32 v75, v118, v118
	v_max_f32_e32 v74, v75, v74
	v_max3_f32 v72, v72, v73, v74
	v_max_f32_e32 v73, v121, v121
	v_max_f32_e32 v74, v120, v120
	v_max_f32_e32 v73, v74, v73
	v_max_f32_e32 v74, v123, v123
	v_max_f32_e32 v75, v122, v122
	s_waitcnt lgkmcnt(0)
	v_mfma_f32_16x16x32_bf16 v[68:71], v[208:211], v[96:99], v[68:71]
	v_max_f32_e32 v74, v75, v74
	v_max3_f32 v72, v72, v73, v74
	v_max_f32_e32 v73, v125, v125
	v_max_f32_e32 v74, v124, v124
	v_max_f32_e32 v73, v74, v73
	v_max_f32_e32 v74, v127, v127
	v_max_f32_e32 v75, v126, v126
	v_max_f32_e32 v74, v75, v74
	v_max3_f32 v72, v72, v73, v74
	v_max_f32_e32 v73, v69, v69
	v_max_f32_e32 v74, v68, v68
	v_max_f32_e32 v73, v74, v73
	v_max_f32_e32 v74, v71, v71
	v_max_f32_e32 v75, v70, v70
	v_max_f32_e32 v74, v75, v74
	v_max3_f32 v72, v72, v73, v74
	ds_bpermute_b32 v73, v148, v72
	s_mov_b32 m0, s51
	v_mov_b32_e32 v135, v130
	buffer_load_dwordx4 v141, s[8:11], s49 offen lds
	s_mov_b32 m0, s52
	s_waitcnt lgkmcnt(0)
	v_max_f32_e32 v73, v73, v73
	v_max_f32_e32 v72, v72, v73
	ds_bpermute_b32 v73, v149, v72
	buffer_load_dwordx4 v142, s[8:11], s49 offen lds
	s_mov_b32 m0, s53
	s_waitcnt lgkmcnt(0)
	v_max_f32_e32 v73, v73, v73
	v_max_f32_e32 v72, v72, v73
	v_sub_f32_e32 v44, v44, v72
	v_sub_f32_e32 v40, v40, v72
	v_exp_f32_e32 v74, v44
	v_sub_f32_e32 v44, v60, v72
	v_exp_f32_e32 v98, v40
	v_sub_f32_e32 v40, v56, v72
	v_exp_f32_e32 v75, v44
	v_sub_f32_e32 v44, v45, v72
	v_exp_f32_e32 v99, v40
	v_sub_f32_e32 v40, v41, v72
	v_exp_f32_e32 v76, v44
	v_sub_f32_e32 v44, v61, v72
	v_sub_f32_e32 v36, v36, v72
	v_exp_f32_e32 v189, v40
	v_sub_f32_e32 v40, v57, v72
	v_exp_f32_e32 v77, v44
	v_sub_f32_e32 v44, v46, v72
	v_exp_f32_e32 v60, v36
	v_sub_f32_e32 v36, v52, v72
	v_exp_f32_e32 v190, v40
	v_sub_f32_e32 v40, v42, v72
	v_exp_f32_e32 v78, v44
	v_sub_f32_e32 v44, v62, v72
	v_exp_f32_e32 v62, v36
	v_sub_f32_e32 v36, v37, v72
	v_exp_f32_e32 v191, v40
	v_sub_f32_e32 v40, v58, v72
	v_exp_f32_e32 v84, v36
	v_sub_f32_e32 v36, v53, v72
	v_exp_f32_e32 v192, v40
	v_sub_f32_e32 v40, v43, v72
	v_exp_f32_e32 v82, v36
	v_sub_f32_e32 v36, v38, v72
	v_exp_f32_e32 v193, v40
	v_sub_f32_e32 v40, v59, v72
	v_exp_f32_e32 v79, v44
	v_sub_f32_e32 v44, v47, v72
	v_exp_f32_e32 v61, v36
	v_sub_f32_e32 v36, v54, v72
	v_exp_f32_e32 v194, v40
	v_sub_f32_e32 v40, v48, v72
	v_exp_f32_e32 v80, v44
	v_sub_f32_e32 v44, v63, v72
	v_exp_f32_e32 v63, v36
	v_sub_f32_e32 v36, v39, v72
	v_exp_f32_e32 v195, v40
	v_sub_f32_e32 v40, v64, v72
	v_exp_f32_e32 v85, v36
	v_sub_f32_e32 v36, v55, v72
	v_exp_f32_e32 v55, v40
	v_sub_f32_e32 v40, v49, v72
	v_exp_f32_e32 v131, v40
	v_sub_f32_e32 v40, v65, v72
	v_exp_f32_e32 v81, v44
	v_exp_f32_e32 v59, v40
	v_sub_f32_e32 v40, v50, v72
	v_exp_f32_e32 v83, v36
	v_exp_f32_e32 v196, v40
	v_sub_f32_e32 v40, v66, v72
	v_exp_f32_e32 v57, v40
	v_sub_f32_e32 v40, v51, v72
	v_exp_f32_e32 v197, v40
	v_pk_add_f32 v[44:45], v[74:75], v[76:77]
	v_pk_add_f32 v[46:47], v[78:79], v[80:81]
	v_sub_f32_e32 v40, v67, v72
	v_pk_add_f32 v[44:45], v[44:45], v[46:47]
	v_pk_add_f32 v[36:37], v[60:61], v[84:85]
	v_pk_add_f32 v[38:39], v[62:63], v[82:83]
	v_exp_f32_e32 v87, v40
	v_pk_add_f32 v[40:41], v[44:45], v[44:45] op_sel:[0,1] op_sel_hi:[1,0]
	v_pk_add_f32 v[36:37], v[36:37], v[36:37] op_sel:[0,1] op_sel_hi:[1,0]
	v_pk_add_f32 v[38:39], v[38:39], v[38:39] op_sel:[0,1] op_sel_hi:[1,0]
	v_mov_b32_e32 v41, v195
	v_mov_b32_e32 v37, v196
	v_mov_b32_e32 v39, v197
	v_add_f32_e32 v54, v98, v189
	v_add_f32_e32 v58, v191, v193
	v_add_f32_e32 v56, v99, v190
	v_add_f32_e32 v86, v192, v194
	v_pk_add_f32 v[40:41], v[40:41], v[130:131]
	v_pk_add_f32 v[36:37], v[36:37], v[38:39]
	v_pk_add_f32 v[38:39], v[54:55], v[58:59]
	v_pk_add_f32 v[36:37], v[40:41], v[36:37]
	v_pk_add_f32 v[40:41], v[56:57], v[86:87]
	buffer_load_dwordx4 v143, s[8:11], s49 offen lds
	v_pk_add_f32 v[38:39], v[38:39], v[40:41]
	s_mov_b32 m0, s54
	v_pk_add_f32 v[36:37], v[36:37], v[38:39]
	v_sub_f32_e32 v38, v100, v72
	v_exp_f32_e32 v50, v38
	v_sub_f32_e32 v38, v104, v72
	v_exp_f32_e32 v51, v38
	v_sub_f32_e32 v38, v101, v72
	v_exp_f32_e32 v52, v38
	v_sub_f32_e32 v38, v105, v72
	v_exp_f32_e32 v53, v38
	v_sub_f32_e32 v38, v102, v72
	v_exp_f32_e32 v64, v38
	v_sub_f32_e32 v38, v106, v72
	v_exp_f32_e32 v65, v38
	v_sub_f32_e32 v38, v103, v72
	v_exp_f32_e32 v66, v38
	v_sub_f32_e32 v38, v107, v72
	v_exp_f32_e32 v67, v38
	v_pk_add_f32 v[38:39], v[50:51], v[52:53]
	buffer_load_dwordx4 v144, s[8:11], s49 offen lds
	s_mov_b32 m0, s55
	v_pk_add_f32 v[40:41], v[64:65], v[66:67]
	buffer_load_dwordx4 v145, s[8:11], s49 offen lds
	v_pk_add_f32 v[38:39], v[38:39], v[40:41]
	v_sub_f32_e32 v40, v108, v72
	v_exp_f32_e32 v44, v40
	v_sub_f32_e32 v40, v112, v72
	v_exp_f32_e32 v46, v40
	v_sub_f32_e32 v40, v109, v72
	v_exp_f32_e32 v48, v40
	v_sub_f32_e32 v40, v113, v72
	v_exp_f32_e32 v88, v40
	v_sub_f32_e32 v40, v110, v72
	v_exp_f32_e32 v45, v40
	v_sub_f32_e32 v40, v114, v72
	v_exp_f32_e32 v47, v40
	v_sub_f32_e32 v40, v111, v72
	v_exp_f32_e32 v49, v40
	v_sub_f32_e32 v40, v115, v72
	v_exp_f32_e32 v89, v40
	s_mov_b32 m0, s56
	v_pk_add_f32 v[40:41], v[44:45], v[48:49]
	v_cvt_pk_bf16_f32 v44, v44, v48
	v_cvt_pk_bf16_f32 v45, v45, v49
	v_cvt_pk_bf16_f32 v48, v50, v52
	v_cvt_pk_bf16_f32 v49, v64, v66
	v_cvt_pk_bf16_f32 v50, v51, v53
	v_cvt_pk_bf16_f32 v51, v65, v67
	v_cvt_pk_bf16_f32 v64, v74, v76
	v_cvt_pk_bf16_f32 v65, v78, v80
	v_cvt_pk_bf16_f32 v66, v75, v77
	v_cvt_pk_bf16_f32 v67, v79, v81
	v_mov_b64_e32 v[76:77], v[2:3]
	v_mov_b64_e32 v[80:81], v[2:3]
	buffer_load_dwordx4 v146, s[8:11], s49 offen lds
	s_mov_b32 m0, s57
	v_mov_b64_e32 v[74:75], v[0:1]
	v_mov_b64_e32 v[78:79], v[0:1]
	buffer_load_dwordx4 v147, s[8:11], s49 offen lds
	v_cvt_pk_bf16_f32 v60, v60, v84
	v_cvt_pk_bf16_f32 v61, v61, v85
	v_cvt_pk_bf16_f32 v62, v62, v82
	v_cvt_pk_bf16_f32 v63, v63, v83
	ds_read_b128 v[82:85], v188
	s_waitcnt lgkmcnt(0)
	v_mfma_f32_16x16x32_bf16 v[74:77], v[82:85], v[4:7], v[74:77]
	v_sub_f32_e32 v73, v121, v72
	v_exp_f32_e32 v86, v73
	v_sub_f32_e32 v73, v118, v72
	v_mfma_f32_16x16x32_bf16 v[78:81], v[82:85], v[64:67], v[78:81]
	ds_read_b128 v[82:85], v187
	v_exp_f32_e32 v100, v73
	v_sub_f32_e32 v73, v122, v72
	v_sub_f32_e32 v68, v68, v72
	v_exp_f32_e32 v101, v73
	v_sub_f32_e32 v73, v119, v72
	v_exp_f32_e32 v91, v68
	v_sub_f32_e32 v68, v125, v72
	v_exp_f32_e32 v102, v73
	v_sub_f32_e32 v73, v123, v72
	v_exp_f32_e32 v105, v68
	v_sub_f32_e32 v68, v69, v72
	v_exp_f32_e32 v103, v73
	v_sub_f32_e32 v73, v124, v72
	v_exp_f32_e32 v93, v68
	v_sub_f32_e32 v68, v126, v72
	v_exp_f32_e32 v104, v73
	v_exp_f32_e32 v69, v68
	v_sub_f32_e32 v68, v70, v72
	v_exp_f32_e32 v95, v68
	v_sub_f32_e32 v68, v127, v72
	s_waitcnt lgkmcnt(0)
	v_mfma_f32_16x16x32_bf16 v[74:77], v[82:85], v[8:11], v[74:77]
	v_sub_f32_e32 v54, v116, v72
	v_sub_f32_e32 v56, v120, v72
	v_sub_f32_e32 v58, v117, v72
	v_mfma_f32_16x16x32_bf16 v[78:81], v[82:85], v[60:63], v[78:81]
	ds_read_b128 v[82:85], v186
	v_exp_f32_e32 v106, v68
	v_exp_f32_e32 v54, v54
	v_exp_f32_e32 v56, v56
	v_exp_f32_e32 v58, v58
	v_sub_f32_e32 v68, v71, v72
	v_pk_add_f32 v[36:37], v[36:37], v[36:37] op_sel:[0,1] op_sel_hi:[1,0]
	v_pk_add_f32 v[38:39], v[38:39], v[38:39] op_sel:[0,1] op_sel_hi:[1,0]
	v_pk_add_f32 v[42:43], v[46:47], v[88:89]
	v_exp_f32_e32 v97, v68
	v_mov_b32_e32 v37, v104
	v_mov_b32_e32 v39, v105
	v_pk_add_f32 v[36:37], v[36:37], v[38:39]
	v_pk_add_f32 v[38:39], v[40:41], v[40:41] op_sel:[0,1] op_sel_hi:[1,0]
	v_pk_add_f32 v[40:41], v[42:43], v[42:43] op_sel:[0,1] op_sel_hi:[1,0]
	v_mov_b32_e32 v39, v69
	v_mov_b32_e32 v41, v106
	v_add_f32_e32 v90, v54, v58
	v_add_f32_e32 v92, v100, v102
	v_add_f32_e32 v94, v56, v86
	v_add_f32_e32 v96, v101, v103
	v_pk_add_f32 v[38:39], v[38:39], v[40:41]
	v_pk_add_f32 v[40:41], v[94:95], v[96:97]
	v_pk_add_f32 v[36:37], v[36:37], v[38:39]
	v_pk_add_f32 v[38:39], v[90:91], v[92:93]
	v_cvt_pk_bf16_f32 v42, v56, v86
	v_pk_add_f32 v[38:39], v[38:39], v[40:41]
	v_cvt_pk_bf16_f32 v40, v54, v58
	v_cvt_pk_bf16_f32 v54, v55, v59
	v_cvt_pk_bf16_f32 v55, v57, v87
	v_cvt_pk_bf16_f32 v56, v98, v189
	v_cvt_pk_bf16_f32 v57, v191, v193
	v_cvt_pk_bf16_f32 v58, v99, v190
	v_cvt_pk_bf16_f32 v59, v192, v194
	s_waitcnt lgkmcnt(0)
	v_mfma_f32_16x16x32_bf16 v[74:77], v[82:85], v[12:15], v[74:77]
	v_cvt_pk_bf16_f32 v52, v195, v131
	v_cvt_pk_bf16_f32 v53, v196, v197
	v_cvt_pk_bf16_f32 v46, v46, v88
	v_mfma_f32_16x16x32_bf16 v[78:81], v[82:85], v[56:59], v[78:81]
	ds_read_b128 v[82:85], v137
	v_cvt_pk_bf16_f32 v47, v47, v89
	v_pk_add_f32 v[36:37], v[36:37], v[38:39]
	s_waitcnt lgkmcnt(0)
	v_mfma_f32_16x16x32_bf16 v[74:77], v[82:85], v[16:19], v[74:77]
	v_add_f32_e32 v36, v36, v37
	ds_bpermute_b32 v37, v148, v36
	v_cvt_pk_bf16_f32 v41, v100, v102
	v_mfma_f32_16x16x32_bf16 v[78:81], v[82:85], v[52:55], v[78:81]
	ds_read_b128 v[82:85], v188 offset:256
	v_cvt_pk_bf16_f32 v43, v101, v103
	s_waitcnt lgkmcnt(1)
	v_add_f32_e32 v36, v36, v37
	s_waitcnt lgkmcnt(0)
	v_mfma_f32_16x16x32_bf16 v[74:77], v[82:85], v[20:23], v[74:77]
	ds_bpermute_b32 v37, v149, v36
	v_cvt_pk_bf16_f32 v38, v91, v93
	v_cvt_pk_bf16_f32 v39, v95, v97
	v_mfma_f32_16x16x32_bf16 v[78:81], v[82:85], v[48:51], v[78:81]
	ds_read_b128 v[82:85], v187 offset:256
	s_waitcnt lgkmcnt(1)
	v_add_f32_e32 v36, v36, v37
	v_rcp_f32_e32 v68, v36
	s_waitcnt lgkmcnt(0)
	v_mfma_f32_16x16x32_bf16 v[74:77], v[82:85], v[24:27], v[74:77]
	v_lshl_add_u64 v[36:37], s[24:25], 0, v[138:139]
	v_lshl_add_u64 v[36:37], v[36:37], 0, s[2:3]
	v_lshl_add_u64 v[70:71], v[36:37], 0, v[134:135]
	v_mfma_f32_16x16x32_bf16 v[78:81], v[82:85], v[44:47], v[78:81]
	ds_read_b128 v[82:85], v186 offset:256
	v_cvt_pk_bf16_f32 v36, v104, v105
	v_cvt_pk_bf16_f32 v37, v69, v106
	s_waitcnt lgkmcnt(0)
	v_mfma_f32_16x16x32_bf16 v[74:77], v[82:85], v[28:31], v[74:77]
	v_lshl_add_u64 v[72:73], v[70:71], 0, s[26:27]
	s_bfe_i32 s8, s0, 0x80000
	s_bfe_u32 s8, s8, 0x5000a
	v_mfma_f32_16x16x32_bf16 v[78:81], v[82:85], v[40:43], v[78:81]
	ds_read_b128 v[82:85], v137 offset:256
	s_add_i32 s0, s0, s8
	s_bfe_i32 s0, s0, 0x80000
	s_waitcnt lgkmcnt(0)
	v_mfma_f32_16x16x32_bf16 v[74:77], v[82:85], v[32:35], v[74:77]
	s_sext_i32_i16 s0, s0
	s_ashr_i32 s0, s0, 5
	s_cmpk_lt_i32 s20, 0x200
	v_mfma_f32_16x16x32_bf16 v[78:81], v[82:85], v[36:39], v[78:81]
	s_nop 3
	v_mul_f32_e64 v74, v74, v136
	v_mul_f32_e64 v75, v75, v136
	v_pk_mul_f32 v[76:77], v[76:77], v[136:137] op_sel_hi:[1,0]
	v_cvt_pk_bf16_f32 v74, v74, v75
	v_cvt_pk_bf16_f32 v75, v76, v77
	global_store_dwordx2 v[70:71], v[74:75], off
	v_pk_mul_f32 v[76:77], v[78:79], v[68:69] op_sel_hi:[1,0]
	v_pk_mul_f32 v[78:79], v[80:81], v[68:69] op_sel_hi:[1,0]
	v_add_co_u32_e64 v74, s[2:3], s60, v70
	v_cvt_pk_bf16_f32 v76, v76, v77
	v_cvt_pk_bf16_f32 v77, v78, v79
	v_addc_co_u32_e64 v75, s[2:3], 0, v71, s[2:3]
	global_store_dwordx2 v[74:75], v[76:77], off
	v_mov_b64_e32 v[76:77], v[2:3]
	v_mov_b64_e32 v[80:81], v[2:3]
	v_mov_b64_e32 v[74:75], v[0:1]
	v_mov_b64_e32 v[78:79], v[0:1]
	ds_read_b128 v[220:223], v188 offset:8192
	ds_read_b128 v[224:227], v187 offset:8192
	ds_read_b128 v[228:231], v186 offset:8192
	ds_read_b128 v[232:235], v137 offset:8192
	ds_read_b128 v[236:239], v188 offset:8448
	ds_read_b128 v[240:243], v187 offset:8448
	s_waitcnt lgkmcnt(5)
	v_mfma_f32_16x16x32_bf16 v[74:77], v[220:223], v[4:7], v[74:77]
	s_cselect_b64 s[8:9], -1, 0
	s_and_b64 vcc, s[8:9], exec
	s_cselect_b32 s0, s0, s13
	v_mfma_f32_16x16x32_bf16 v[78:81], v[220:223], v[64:67], v[78:81]
	ds_read_b128 v[244:247], v186 offset:8448
	s_cselect_b32 s1, s1, s12
	s_lshl_b32 s0, s0, 2
	s_waitcnt lgkmcnt(5)
	v_mfma_f32_16x16x32_bf16 v[74:77], v[224:227], v[8:11], v[74:77]
	s_add_i32 s0, s0, s1
	s_ashr_i32 s1, s0, 31
	s_lshl_b64 s[0:1], s[0:1], 17
	v_mfma_f32_16x16x32_bf16 v[78:81], v[224:227], v[60:63], v[78:81]
	ds_read_b128 v[248:251], v137 offset:8448
	s_add_u32 s12, s7, s0
	s_addc_u32 s0, s28, s1
	s_waitcnt lgkmcnt(5)
	v_mfma_f32_16x16x32_bf16 v[74:77], v[228:231], v[12:15], v[74:77]
	s_and_b32 s13, s0, 0xffff
	v_mfma_f32_16x16x32_bf16 v[78:81], v[228:231], v[56:59], v[78:81]
	ds_read_b128 v[220:223], v188 offset:16384
	s_waitcnt lgkmcnt(5)
	v_mfma_f32_16x16x32_bf16 v[74:77], v[232:235], v[16:19], v[74:77]
	v_mfma_f32_16x16x32_bf16 v[78:81], v[232:235], v[52:55], v[78:81]
	ds_read_b128 v[224:227], v187 offset:16384
	s_waitcnt lgkmcnt(5)
	v_mfma_f32_16x16x32_bf16 v[74:77], v[236:239], v[20:23], v[74:77]
	v_mfma_f32_16x16x32_bf16 v[78:81], v[236:239], v[48:51], v[78:81]
	ds_read_b128 v[228:231], v186 offset:16384
	s_waitcnt lgkmcnt(5)
	v_mfma_f32_16x16x32_bf16 v[74:77], v[240:243], v[24:27], v[74:77]
	v_mfma_f32_16x16x32_bf16 v[78:81], v[240:243], v[44:47], v[78:81]
	ds_read_b128 v[232:235], v137 offset:16384
	s_waitcnt lgkmcnt(5)
	v_mfma_f32_16x16x32_bf16 v[74:77], v[244:247], v[28:31], v[74:77]
	v_mfma_f32_16x16x32_bf16 v[78:81], v[244:247], v[40:43], v[78:81]
	ds_read_b128 v[236:239], v188 offset:16640
	s_waitcnt lgkmcnt(5)
	v_mfma_f32_16x16x32_bf16 v[74:77], v[248:251], v[32:35], v[74:77]
	s_nop 7
	v_pk_mul_f32 v[74:75], v[74:75], v[136:137] op_sel_hi:[1,0]
	v_mfma_f32_16x16x32_bf16 v[78:81], v[248:251], v[36:39], v[78:81]
	ds_read_b128 v[240:243], v187 offset:16640
	v_mul_f32_e64 v76, v76, v136
	v_mul_f32_e64 v77, v77, v136
	v_cvt_pk_bf16_f32 v74, v74, v75
	v_cvt_pk_bf16_f32 v75, v76, v77
	s_nop 3
	v_pk_mul_f32 v[76:77], v[78:79], v[68:69] op_sel_hi:[1,0]
	v_pk_mul_f32 v[78:79], v[80:81], v[68:69] op_sel_hi:[1,0]
	v_cvt_pk_bf16_f32 v76, v76, v77
	v_cvt_pk_bf16_f32 v77, v78, v79
	global_store_dwordx2 v[70:71], v[74:75], off offset:32
	global_store_dwordx2 v[72:73], v[76:77], off offset:32
	v_mov_b64_e32 v[76:77], v[2:3]
	v_mov_b64_e32 v[80:81], v[2:3]
	v_mov_b64_e32 v[74:75], v[0:1]
	v_mov_b64_e32 v[78:79], v[0:1]
	s_waitcnt lgkmcnt(5)
	v_mfma_f32_16x16x32_bf16 v[74:77], v[220:223], v[4:7], v[74:77]
	v_mfma_f32_16x16x32_bf16 v[78:81], v[220:223], v[64:67], v[78:81]
	ds_read_b128 v[244:247], v186 offset:16640
	s_waitcnt lgkmcnt(5)
	v_mfma_f32_16x16x32_bf16 v[74:77], v[224:227], v[8:11], v[74:77]
	v_mfma_f32_16x16x32_bf16 v[78:81], v[224:227], v[60:63], v[78:81]
	ds_read_b128 v[248:251], v137 offset:16640
	s_waitcnt lgkmcnt(5)
	v_mfma_f32_16x16x32_bf16 v[74:77], v[228:231], v[12:15], v[74:77]
	v_mfma_f32_16x16x32_bf16 v[78:81], v[228:231], v[56:59], v[78:81]
	ds_read_b128 v[220:223], v188 offset:24576
	s_waitcnt lgkmcnt(5)
	v_mfma_f32_16x16x32_bf16 v[74:77], v[232:235], v[16:19], v[74:77]
	v_mfma_f32_16x16x32_bf16 v[78:81], v[232:235], v[52:55], v[78:81]
	ds_read_b128 v[224:227], v187 offset:24576
	s_waitcnt lgkmcnt(5)
	v_mfma_f32_16x16x32_bf16 v[74:77], v[236:239], v[20:23], v[74:77]
	v_mfma_f32_16x16x32_bf16 v[78:81], v[236:239], v[48:51], v[78:81]
	ds_read_b128 v[228:231], v186 offset:24576
	s_waitcnt lgkmcnt(5)
	v_mfma_f32_16x16x32_bf16 v[74:77], v[240:243], v[24:27], v[74:77]
	v_mfma_f32_16x16x32_bf16 v[78:81], v[240:243], v[44:47], v[78:81]
	ds_read_b128 v[232:235], v137 offset:24576
	s_waitcnt lgkmcnt(5)
	v_mfma_f32_16x16x32_bf16 v[74:77], v[244:247], v[28:31], v[74:77]
	v_mfma_f32_16x16x32_bf16 v[78:81], v[244:247], v[40:43], v[78:81]
	ds_read_b128 v[236:239], v188 offset:24832
	s_waitcnt lgkmcnt(5)
	v_mfma_f32_16x16x32_bf16 v[74:77], v[248:251], v[32:35], v[74:77]
	s_nop 7
	v_pk_mul_f32 v[74:75], v[74:75], v[136:137] op_sel_hi:[1,0]
	v_mfma_f32_16x16x32_bf16 v[78:81], v[248:251], v[36:39], v[78:81]
	ds_read_b128 v[240:243], v187 offset:24832
	v_mul_f32_e64 v76, v76, v136
	v_mul_f32_e64 v77, v77, v136
	v_cvt_pk_bf16_f32 v74, v74, v75
	v_cvt_pk_bf16_f32 v75, v76, v77
	s_nop 3
	v_pk_mul_f32 v[76:77], v[78:79], v[68:69] op_sel_hi:[1,0]
	v_pk_mul_f32 v[78:79], v[80:81], v[68:69] op_sel_hi:[1,0]
	v_cvt_pk_bf16_f32 v76, v76, v77
	v_cvt_pk_bf16_f32 v77, v78, v79
	global_store_dwordx2 v[70:71], v[74:75], off offset:64
	global_store_dwordx2 v[72:73], v[76:77], off offset:64
	v_mov_b64_e32 v[76:77], v[2:3]
	v_mov_b64_e32 v[80:81], v[2:3]
	v_mov_b64_e32 v[74:75], v[0:1]
	v_mov_b64_e32 v[78:79], v[0:1]
	s_waitcnt lgkmcnt(5)
	v_mfma_f32_16x16x32_bf16 v[74:77], v[220:223], v[4:7], v[74:77]
	v_mfma_f32_16x16x32_bf16 v[78:81], v[220:223], v[64:67], v[78:81]
	ds_read_b128 v[244:247], v186 offset:24832
	s_waitcnt lgkmcnt(5)
	v_mfma_f32_16x16x32_bf16 v[74:77], v[224:227], v[8:11], v[74:77]
	v_mfma_f32_16x16x32_bf16 v[78:81], v[224:227], v[60:63], v[78:81]
	ds_read_b128 v[248:251], v137 offset:24832
	s_waitcnt lgkmcnt(5)
	v_mfma_f32_16x16x32_bf16 v[74:77], v[228:231], v[12:15], v[74:77]
	v_mfma_f32_16x16x32_bf16 v[78:81], v[228:231], v[56:59], v[78:81]
	ds_read_b128 v[220:223], v188 offset:32768
	s_waitcnt lgkmcnt(5)
	v_mfma_f32_16x16x32_bf16 v[74:77], v[232:235], v[16:19], v[74:77]
	v_mfma_f32_16x16x32_bf16 v[78:81], v[232:235], v[52:55], v[78:81]
	ds_read_b128 v[224:227], v187 offset:32768
	s_waitcnt lgkmcnt(5)
	v_mfma_f32_16x16x32_bf16 v[74:77], v[236:239], v[20:23], v[74:77]
	v_mfma_f32_16x16x32_bf16 v[78:81], v[236:239], v[48:51], v[78:81]
	ds_read_b128 v[228:231], v186 offset:32768
	s_waitcnt lgkmcnt(5)
	v_mfma_f32_16x16x32_bf16 v[74:77], v[240:243], v[24:27], v[74:77]
	v_mfma_f32_16x16x32_bf16 v[78:81], v[240:243], v[44:47], v[78:81]
	ds_read_b128 v[232:235], v137 offset:32768
	s_waitcnt lgkmcnt(5)
	v_mfma_f32_16x16x32_bf16 v[74:77], v[244:247], v[28:31], v[74:77]
	v_mfma_f32_16x16x32_bf16 v[78:81], v[244:247], v[40:43], v[78:81]
	ds_read_b128 v[236:239], v188 offset:33024
	s_waitcnt lgkmcnt(5)
	v_mfma_f32_16x16x32_bf16 v[74:77], v[248:251], v[32:35], v[74:77]
	s_nop 7
	v_pk_mul_f32 v[74:75], v[74:75], v[136:137] op_sel_hi:[1,0]
	v_mfma_f32_16x16x32_bf16 v[78:81], v[248:251], v[36:39], v[78:81]
	ds_read_b128 v[240:243], v187 offset:33024
	v_mul_f32_e64 v76, v76, v136
	v_mul_f32_e64 v77, v77, v136
	v_cvt_pk_bf16_f32 v74, v74, v75
	v_cvt_pk_bf16_f32 v75, v76, v77
	s_nop 3
	v_pk_mul_f32 v[76:77], v[78:79], v[68:69] op_sel_hi:[1,0]
	v_pk_mul_f32 v[78:79], v[80:81], v[68:69] op_sel_hi:[1,0]
	v_cvt_pk_bf16_f32 v76, v76, v77
	v_cvt_pk_bf16_f32 v77, v78, v79
	global_store_dwordx2 v[70:71], v[74:75], off offset:96
	global_store_dwordx2 v[72:73], v[76:77], off offset:96
	v_mov_b64_e32 v[76:77], v[2:3]
	v_mov_b64_e32 v[80:81], v[2:3]
	v_mov_b64_e32 v[74:75], v[0:1]
	v_mov_b64_e32 v[78:79], v[0:1]
	s_waitcnt lgkmcnt(5)
	v_mfma_f32_16x16x32_bf16 v[74:77], v[220:223], v[4:7], v[74:77]
	v_mfma_f32_16x16x32_bf16 v[78:81], v[220:223], v[64:67], v[78:81]
	ds_read_b128 v[244:247], v186 offset:33024
	s_waitcnt lgkmcnt(5)
	v_mfma_f32_16x16x32_bf16 v[74:77], v[224:227], v[8:11], v[74:77]
	v_mfma_f32_16x16x32_bf16 v[78:81], v[224:227], v[60:63], v[78:81]
	ds_read_b128 v[248:251], v137 offset:33024
	s_waitcnt lgkmcnt(5)
	v_mfma_f32_16x16x32_bf16 v[74:77], v[228:231], v[12:15], v[74:77]
	v_mfma_f32_16x16x32_bf16 v[78:81], v[228:231], v[56:59], v[78:81]
	ds_read_b128 v[220:223], v188 offset:40960
	s_waitcnt lgkmcnt(5)
	v_mfma_f32_16x16x32_bf16 v[74:77], v[232:235], v[16:19], v[74:77]
	v_mfma_f32_16x16x32_bf16 v[78:81], v[232:235], v[52:55], v[78:81]
	ds_read_b128 v[224:227], v187 offset:40960
	s_waitcnt lgkmcnt(5)
	v_mfma_f32_16x16x32_bf16 v[74:77], v[236:239], v[20:23], v[74:77]
	v_mfma_f32_16x16x32_bf16 v[78:81], v[236:239], v[48:51], v[78:81]
	ds_read_b128 v[228:231], v186 offset:40960
	s_waitcnt lgkmcnt(5)
	v_mfma_f32_16x16x32_bf16 v[74:77], v[240:243], v[24:27], v[74:77]
	v_mfma_f32_16x16x32_bf16 v[78:81], v[240:243], v[44:47], v[78:81]
	ds_read_b128 v[232:235], v137 offset:40960
	s_waitcnt lgkmcnt(5)
	v_mfma_f32_16x16x32_bf16 v[74:77], v[244:247], v[28:31], v[74:77]
	v_mfma_f32_16x16x32_bf16 v[78:81], v[244:247], v[40:43], v[78:81]
	ds_read_b128 v[236:239], v188 offset:41216
	s_waitcnt lgkmcnt(5)
	v_mfma_f32_16x16x32_bf16 v[74:77], v[248:251], v[32:35], v[74:77]
	s_nop 7
	v_pk_mul_f32 v[74:75], v[74:75], v[136:137] op_sel_hi:[1,0]
	v_mfma_f32_16x16x32_bf16 v[78:81], v[248:251], v[36:39], v[78:81]
	ds_read_b128 v[240:243], v187 offset:41216
	v_mul_f32_e64 v76, v76, v136
	v_mul_f32_e64 v77, v77, v136
	v_cvt_pk_bf16_f32 v74, v74, v75
	v_cvt_pk_bf16_f32 v75, v76, v77
	s_nop 3
	v_pk_mul_f32 v[76:77], v[78:79], v[68:69] op_sel_hi:[1,0]
	v_pk_mul_f32 v[78:79], v[80:81], v[68:69] op_sel_hi:[1,0]
	v_cvt_pk_bf16_f32 v76, v76, v77
	v_cvt_pk_bf16_f32 v77, v78, v79
	global_store_dwordx2 v[70:71], v[74:75], off offset:128
	global_store_dwordx2 v[72:73], v[76:77], off offset:128
	v_mov_b64_e32 v[76:77], v[2:3]
	v_mov_b64_e32 v[80:81], v[2:3]
	v_mov_b64_e32 v[74:75], v[0:1]
	v_mov_b64_e32 v[78:79], v[0:1]
	s_waitcnt lgkmcnt(5)
	v_mfma_f32_16x16x32_bf16 v[74:77], v[220:223], v[4:7], v[74:77]
	v_mfma_f32_16x16x32_bf16 v[78:81], v[220:223], v[64:67], v[78:81]
	ds_read_b128 v[244:247], v186 offset:41216
	s_waitcnt lgkmcnt(5)
	v_mfma_f32_16x16x32_bf16 v[74:77], v[224:227], v[8:11], v[74:77]
	v_mfma_f32_16x16x32_bf16 v[78:81], v[224:227], v[60:63], v[78:81]
	ds_read_b128 v[248:251], v137 offset:41216
	s_waitcnt lgkmcnt(5)
	v_mfma_f32_16x16x32_bf16 v[74:77], v[228:231], v[12:15], v[74:77]
	v_mfma_f32_16x16x32_bf16 v[78:81], v[228:231], v[56:59], v[78:81]
	ds_read_b128 v[220:223], v188 offset:49152
	s_waitcnt lgkmcnt(5)
	v_mfma_f32_16x16x32_bf16 v[74:77], v[232:235], v[16:19], v[74:77]
	v_mfma_f32_16x16x32_bf16 v[78:81], v[232:235], v[52:55], v[78:81]
	ds_read_b128 v[224:227], v187 offset:49152
	s_waitcnt lgkmcnt(5)
	v_mfma_f32_16x16x32_bf16 v[74:77], v[236:239], v[20:23], v[74:77]
	v_mfma_f32_16x16x32_bf16 v[78:81], v[236:239], v[48:51], v[78:81]
	ds_read_b128 v[228:231], v186 offset:49152
	s_waitcnt lgkmcnt(5)
	v_mfma_f32_16x16x32_bf16 v[74:77], v[240:243], v[24:27], v[74:77]
	v_mfma_f32_16x16x32_bf16 v[78:81], v[240:243], v[44:47], v[78:81]
	ds_read_b128 v[232:235], v137 offset:49152
	s_waitcnt lgkmcnt(5)
	v_mfma_f32_16x16x32_bf16 v[74:77], v[244:247], v[28:31], v[74:77]
	v_mfma_f32_16x16x32_bf16 v[78:81], v[244:247], v[40:43], v[78:81]
	ds_read_b128 v[236:239], v188 offset:49408
	s_waitcnt lgkmcnt(5)
	v_mfma_f32_16x16x32_bf16 v[74:77], v[248:251], v[32:35], v[74:77]
	s_nop 7
	v_pk_mul_f32 v[74:75], v[74:75], v[136:137] op_sel_hi:[1,0]
	v_mfma_f32_16x16x32_bf16 v[78:81], v[248:251], v[36:39], v[78:81]
	ds_read_b128 v[240:243], v187 offset:49408
	v_mul_f32_e64 v76, v76, v136
	v_mul_f32_e64 v77, v77, v136
	v_cvt_pk_bf16_f32 v74, v74, v75
	v_cvt_pk_bf16_f32 v75, v76, v77
	s_nop 3
	v_pk_mul_f32 v[76:77], v[78:79], v[68:69] op_sel_hi:[1,0]
	v_pk_mul_f32 v[78:79], v[80:81], v[68:69] op_sel_hi:[1,0]
	v_cvt_pk_bf16_f32 v76, v76, v77
	v_cvt_pk_bf16_f32 v77, v78, v79
	global_store_dwordx2 v[70:71], v[74:75], off offset:160
	global_store_dwordx2 v[72:73], v[76:77], off offset:160
	v_mov_b64_e32 v[76:77], v[2:3]
	v_mov_b64_e32 v[80:81], v[2:3]
	v_mov_b64_e32 v[74:75], v[0:1]
	v_mov_b64_e32 v[78:79], v[0:1]
	s_waitcnt lgkmcnt(5)
	v_mfma_f32_16x16x32_bf16 v[74:77], v[220:223], v[4:7], v[74:77]
	v_mfma_f32_16x16x32_bf16 v[78:81], v[220:223], v[64:67], v[78:81]
	ds_read_b128 v[244:247], v186 offset:49408
	s_waitcnt lgkmcnt(5)
	v_mfma_f32_16x16x32_bf16 v[74:77], v[224:227], v[8:11], v[74:77]
	v_mfma_f32_16x16x32_bf16 v[78:81], v[224:227], v[60:63], v[78:81]
	ds_read_b128 v[248:251], v137 offset:49408
	s_waitcnt lgkmcnt(5)
	v_mfma_f32_16x16x32_bf16 v[74:77], v[228:231], v[12:15], v[74:77]
	v_mfma_f32_16x16x32_bf16 v[78:81], v[228:231], v[56:59], v[78:81]
	ds_read_b128 v[220:223], v188 offset:57344
	s_waitcnt lgkmcnt(5)
	v_mfma_f32_16x16x32_bf16 v[74:77], v[232:235], v[16:19], v[74:77]
	v_mfma_f32_16x16x32_bf16 v[78:81], v[232:235], v[52:55], v[78:81]
	ds_read_b128 v[224:227], v187 offset:57344
	s_waitcnt lgkmcnt(5)
	v_mfma_f32_16x16x32_bf16 v[74:77], v[236:239], v[20:23], v[74:77]
	v_mfma_f32_16x16x32_bf16 v[78:81], v[236:239], v[48:51], v[78:81]
	ds_read_b128 v[228:231], v186 offset:57344
	s_waitcnt lgkmcnt(5)
	v_mfma_f32_16x16x32_bf16 v[74:77], v[240:243], v[24:27], v[74:77]
	v_mfma_f32_16x16x32_bf16 v[78:81], v[240:243], v[44:47], v[78:81]
	ds_read_b128 v[232:235], v137 offset:57344
	s_waitcnt lgkmcnt(5)
	v_mfma_f32_16x16x32_bf16 v[74:77], v[244:247], v[28:31], v[74:77]
	v_mfma_f32_16x16x32_bf16 v[78:81], v[244:247], v[40:43], v[78:81]
	ds_read_b128 v[236:239], v188 offset:57600
	s_waitcnt lgkmcnt(5)
	v_mfma_f32_16x16x32_bf16 v[74:77], v[248:251], v[32:35], v[74:77]
	s_nop 7
	v_pk_mul_f32 v[74:75], v[74:75], v[136:137] op_sel_hi:[1,0]
	v_mfma_f32_16x16x32_bf16 v[78:81], v[248:251], v[36:39], v[78:81]
	ds_read_b128 v[240:243], v187 offset:57600
	v_mul_f32_e64 v76, v76, v136
	v_mul_f32_e64 v77, v77, v136
	v_cvt_pk_bf16_f32 v74, v74, v75
	v_cvt_pk_bf16_f32 v75, v76, v77
	s_nop 3
	v_pk_mul_f32 v[76:77], v[78:79], v[68:69] op_sel_hi:[1,0]
	v_pk_mul_f32 v[78:79], v[80:81], v[68:69] op_sel_hi:[1,0]
	v_cvt_pk_bf16_f32 v76, v76, v77
	v_cvt_pk_bf16_f32 v77, v78, v79
	global_store_dwordx2 v[70:71], v[74:75], off offset:192
	global_store_dwordx2 v[72:73], v[76:77], off offset:192
	v_mov_b64_e32 v[76:77], v[2:3]
	v_mov_b64_e32 v[80:81], v[2:3]
	v_mov_b64_e32 v[74:75], v[0:1]
	v_mov_b64_e32 v[78:79], v[0:1]
	s_waitcnt lgkmcnt(5)
	v_mfma_f32_16x16x32_bf16 v[74:77], v[220:223], v[4:7], v[74:77]
	v_mfma_f32_16x16x32_bf16 v[78:81], v[220:223], v[64:67], v[78:81]
	ds_read_b128 v[244:247], v186 offset:57600
	s_waitcnt lgkmcnt(5)
	v_mfma_f32_16x16x32_bf16 v[74:77], v[224:227], v[8:11], v[74:77]
	v_mfma_f32_16x16x32_bf16 v[78:81], v[224:227], v[60:63], v[78:81]
	ds_read_b128 v[248:251], v137 offset:57600
	s_waitcnt lgkmcnt(5)
	v_mfma_f32_16x16x32_bf16 v[74:77], v[228:231], v[12:15], v[74:77]
	v_mfma_f32_16x16x32_bf16 v[78:81], v[228:231], v[56:59], v[78:81]
	s_waitcnt lgkmcnt(4)
	v_mfma_f32_16x16x32_bf16 v[74:77], v[232:235], v[16:19], v[74:77]
	v_mfma_f32_16x16x32_bf16 v[78:81], v[232:235], v[52:55], v[78:81]
	s_waitcnt lgkmcnt(3)
	v_mfma_f32_16x16x32_bf16 v[74:77], v[236:239], v[20:23], v[74:77]
	v_mfma_f32_16x16x32_bf16 v[78:81], v[236:239], v[48:51], v[78:81]
	s_waitcnt lgkmcnt(2)
	v_mfma_f32_16x16x32_bf16 v[74:77], v[240:243], v[24:27], v[74:77]
	v_mfma_f32_16x16x32_bf16 v[78:81], v[240:243], v[44:47], v[78:81]
	s_waitcnt lgkmcnt(1)
	v_mfma_f32_16x16x32_bf16 v[74:77], v[244:247], v[28:31], v[74:77]
	v_mfma_f32_16x16x32_bf16 v[78:81], v[244:247], v[40:43], v[78:81]
	s_waitcnt lgkmcnt(0)
	v_mfma_f32_16x16x32_bf16 v[74:77], v[248:251], v[32:35], v[74:77]
	s_nop 7
	v_pk_mul_f32 v[74:75], v[74:75], v[136:137] op_sel_hi:[1,0]
	v_mfma_f32_16x16x32_bf16 v[78:81], v[248:251], v[36:39], v[78:81]
	v_mul_f32_e64 v76, v76, v136
	v_mul_f32_e64 v77, v77, v136
	v_cvt_pk_bf16_f32 v74, v74, v75
	v_cvt_pk_bf16_f32 v75, v76, v77
	s_nop 3
	v_pk_mul_f32 v[76:77], v[78:79], v[68:69] op_sel_hi:[1,0]
	v_pk_mul_f32 v[78:79], v[80:81], v[68:69] op_sel_hi:[1,0]
	v_cvt_pk_bf16_f32 v76, v76, v77
	v_cvt_pk_bf16_f32 v77, v78, v79
	global_store_dwordx2 v[70:71], v[74:75], off offset:224
	global_store_dwordx2 v[72:73], v[76:77], off offset:224
	s_waitcnt vmcnt(0)
	s_waitcnt lgkmcnt(0)
	s_barrier
	s_cbranch_vccz .LBB0_1069
	s_mov_b32 m0, s29
	s_nop 0
	buffer_load_dwordx4 v140, s[12:15], 0 offen lds
	s_mov_b32 m0, s30
	s_nop 0
	buffer_load_dwordx4 v141, s[12:15], 0 offen lds
	s_mov_b32 m0, s31
	s_nop 0
	buffer_load_dwordx4 v142, s[12:15], 0 offen lds
	s_mov_b32 m0, s35
	s_nop 0
	buffer_load_dwordx4 v143, s[12:15], 0 offen lds
	s_mov_b32 m0, s37
	s_nop 0
	buffer_load_dwordx4 v144, s[12:15], 0 offen lds
	s_mov_b32 m0, s39
	s_nop 0
	buffer_load_dwordx4 v145, s[12:15], 0 offen lds
	s_mov_b32 m0, s41
	s_nop 0
	buffer_load_dwordx4 v146, s[12:15], 0 offen lds
	s_mov_b32 m0, s48
	s_nop 0
	buffer_load_dwordx4 v147, s[12:15], 0 offen lds
.LBB0_1069:
	v_mov_b64_e32 v[76:77], v[2:3]
	v_mov_b64_e32 v[80:81], v[2:3]
	v_mov_b64_e32 v[74:75], v[0:1]
	v_mov_b64_e32 v[78:79], v[0:1]
	v_add_u32_e32 v69, v178, v151
	v_add_u32_e32 v252, v150, v151
	v_add_u32_e32 v252, 0x10000, v252
	v_add_u32_e32 v253, v150, v152
	v_add_u32_e32 v253, 0x10000, v253
	v_add_u32_e32 v254, v150, v153
	v_add_u32_e32 v254, 0x10000, v254
	v_add_u32_e32 v255, v150, v154
	v_add_u32_e32 v255, 0x10000, v255
	ds_read_b128 v[220:223], v252
	ds_read_b128 v[224:227], v253
	ds_read_b128 v[228:231], v254
	ds_read_b128 v[232:235], v255
	ds_read_b128 v[236:239], v252 offset:256
	ds_read_b128 v[240:243], v253 offset:256
	v_add_u32_e32 v69, v178, v152
	v_add_u32_e32 v69, v178, v153
	v_mov_b32_e32 v137, v136
	s_waitcnt lgkmcnt(5)
	v_mfma_f32_16x16x32_bf16 v[74:77], v[220:223], v[4:7], v[74:77]
	s_mov_b64 s[2:3], -1
	s_and_b64 vcc, s[8:9], exec
	v_mfma_f32_16x16x32_bf16 v[78:81], v[220:223], v[64:67], v[78:81]
	ds_read_b128 v[244:247], v254 offset:256
	v_add_u32_e32 v69, v178, v154
	s_waitcnt lgkmcnt(5)
	v_mfma_f32_16x16x32_bf16 v[74:77], v[224:227], v[8:11], v[74:77]
	v_mfma_f32_16x16x32_bf16 v[78:81], v[224:227], v[60:63], v[78:81]
	ds_read_b128 v[248:251], v255 offset:256
	v_add_u32_e32 v69, v178, v155
	s_waitcnt lgkmcnt(5)
	v_mfma_f32_16x16x32_bf16 v[74:77], v[228:231], v[12:15], v[74:77]
	v_mfma_f32_16x16x32_bf16 v[78:81], v[228:231], v[56:59], v[78:81]
	ds_read_b128 v[220:223], v252 offset:8192
	v_add_u32_e32 v69, v178, v156
	s_waitcnt lgkmcnt(5)
	v_mfma_f32_16x16x32_bf16 v[74:77], v[232:235], v[16:19], v[74:77]
	v_mfma_f32_16x16x32_bf16 v[78:81], v[232:235], v[52:55], v[78:81]
	ds_read_b128 v[224:227], v253 offset:8192
	v_add_u32_e32 v69, v178, v157
	s_waitcnt lgkmcnt(5)
	v_mfma_f32_16x16x32_bf16 v[74:77], v[236:239], v[20:23], v[74:77]
	v_mfma_f32_16x16x32_bf16 v[78:81], v[236:239], v[48:51], v[78:81]
	ds_read_b128 v[228:231], v254 offset:8192
	v_add_u32_e32 v69, v178, v158
	s_waitcnt lgkmcnt(5)
	v_mfma_f32_16x16x32_bf16 v[74:77], v[240:243], v[24:27], v[74:77]
	v_mfma_f32_16x16x32_bf16 v[78:81], v[240:243], v[44:47], v[78:81]
	ds_read_b128 v[232:235], v255 offset:8192
	v_mov_b32_e32 v69, v68
	s_waitcnt lgkmcnt(5)
	v_mfma_f32_16x16x32_bf16 v[74:77], v[244:247], v[28:31], v[74:77]
	v_mfma_f32_16x16x32_bf16 v[78:81], v[244:247], v[40:43], v[78:81]
	ds_read_b128 v[236:239], v252 offset:8448
	v_add_u32_e32 v82, v179, v151
	s_waitcnt lgkmcnt(5)
	v_mfma_f32_16x16x32_bf16 v[74:77], v[248:251], v[32:35], v[74:77]
	v_mfma_f32_16x16x32_bf16 v[78:81], v[248:251], v[36:39], v[78:81]
	ds_read_b128 v[240:243], v253 offset:8448
	v_add_u32_e32 v86, v179, v152
	s_nop 5
	v_pk_mul_f32 v[74:75], v[74:75], v[136:137]
	v_pk_mul_f32 v[76:77], v[76:77], v[136:137]
	v_cvt_pk_bf16_f32 v74, v74, v75
	v_cvt_pk_bf16_f32 v75, v76, v77
	v_pk_mul_f32 v[76:77], v[78:79], v[68:69]
	v_pk_mul_f32 v[78:79], v[80:81], v[68:69]
	v_cvt_pk_bf16_f32 v76, v76, v77
	v_cvt_pk_bf16_f32 v77, v78, v79
	global_store_dwordx2 v[70:71], v[74:75], off offset:256
	global_store_dwordx2 v[72:73], v[76:77], off offset:256
	v_mov_b64_e32 v[76:77], v[2:3]
	v_mov_b64_e32 v[80:81], v[2:3]
	v_mov_b64_e32 v[74:75], v[0:1]
	v_mov_b64_e32 v[78:79], v[0:1]
	s_waitcnt lgkmcnt(5)
	v_mfma_f32_16x16x32_bf16 v[74:77], v[220:223], v[4:7], v[74:77]
	v_mfma_f32_16x16x32_bf16 v[78:81], v[220:223], v[64:67], v[78:81]
	ds_read_b128 v[244:247], v254 offset:8448
	v_add_u32_e32 v82, v179, v153
	s_waitcnt lgkmcnt(5)
	v_mfma_f32_16x16x32_bf16 v[74:77], v[224:227], v[8:11], v[74:77]
	v_mfma_f32_16x16x32_bf16 v[78:81], v[224:227], v[60:63], v[78:81]
	ds_read_b128 v[248:251], v255 offset:8448
	v_add_u32_e32 v86, v179, v154
	s_waitcnt lgkmcnt(5)
	v_mfma_f32_16x16x32_bf16 v[74:77], v[228:231], v[12:15], v[74:77]
	v_mfma_f32_16x16x32_bf16 v[78:81], v[228:231], v[56:59], v[78:81]
	ds_read_b128 v[220:223], v252 offset:16384
	v_add_u32_e32 v82, v179, v155
	s_waitcnt lgkmcnt(5)
	v_mfma_f32_16x16x32_bf16 v[74:77], v[232:235], v[16:19], v[74:77]
	v_mfma_f32_16x16x32_bf16 v[78:81], v[232:235], v[52:55], v[78:81]
	ds_read_b128 v[224:227], v253 offset:16384
	v_add_u32_e32 v86, v179, v156
	s_waitcnt lgkmcnt(5)
	v_mfma_f32_16x16x32_bf16 v[74:77], v[236:239], v[20:23], v[74:77]
	v_mfma_f32_16x16x32_bf16 v[78:81], v[236:239], v[48:51], v[78:81]
	ds_read_b128 v[228:231], v254 offset:16384
	v_add_u32_e32 v82, v179, v157
	s_waitcnt lgkmcnt(5)
	v_mfma_f32_16x16x32_bf16 v[74:77], v[240:243], v[24:27], v[74:77]
	v_mfma_f32_16x16x32_bf16 v[78:81], v[240:243], v[44:47], v[78:81]
	ds_read_b128 v[232:235], v255 offset:16384
	v_add_u32_e32 v86, v179, v158
	s_waitcnt lgkmcnt(5)
	v_mfma_f32_16x16x32_bf16 v[74:77], v[244:247], v[28:31], v[74:77]
	v_mfma_f32_16x16x32_bf16 v[78:81], v[244:247], v[40:43], v[78:81]
	ds_read_b128 v[236:239], v252 offset:16640
	v_add_u32_e32 v82, v180, v151
	s_waitcnt lgkmcnt(5)
	v_mfma_f32_16x16x32_bf16 v[74:77], v[248:251], v[32:35], v[74:77]
	v_mfma_f32_16x16x32_bf16 v[78:81], v[248:251], v[36:39], v[78:81]
	ds_read_b128 v[240:243], v253 offset:16640
	v_add_u32_e32 v86, v180, v152
	s_nop 5
	v_pk_mul_f32 v[74:75], v[74:75], v[136:137]
	v_pk_mul_f32 v[76:77], v[76:77], v[136:137]
	v_cvt_pk_bf16_f32 v74, v74, v75
	v_cvt_pk_bf16_f32 v75, v76, v77
	v_pk_mul_f32 v[76:77], v[78:79], v[68:69]
	v_pk_mul_f32 v[78:79], v[80:81], v[68:69]
	v_cvt_pk_bf16_f32 v76, v76, v77
	v_cvt_pk_bf16_f32 v77, v78, v79
	global_store_dwordx2 v[70:71], v[74:75], off offset:288
	global_store_dwordx2 v[72:73], v[76:77], off offset:288
	v_mov_b64_e32 v[76:77], v[2:3]
	v_mov_b64_e32 v[80:81], v[2:3]
	v_mov_b64_e32 v[74:75], v[0:1]
	v_mov_b64_e32 v[78:79], v[0:1]
	s_waitcnt lgkmcnt(5)
	v_mfma_f32_16x16x32_bf16 v[74:77], v[220:223], v[4:7], v[74:77]
	v_mfma_f32_16x16x32_bf16 v[78:81], v[220:223], v[64:67], v[78:81]
	ds_read_b128 v[244:247], v254 offset:16640
	v_add_u32_e32 v82, v180, v153
	s_waitcnt lgkmcnt(5)
	v_mfma_f32_16x16x32_bf16 v[74:77], v[224:227], v[8:11], v[74:77]
	v_mfma_f32_16x16x32_bf16 v[78:81], v[224:227], v[60:63], v[78:81]
	ds_read_b128 v[248:251], v255 offset:16640
	v_add_u32_e32 v86, v180, v154
	s_waitcnt lgkmcnt(5)
	v_mfma_f32_16x16x32_bf16 v[74:77], v[228:231], v[12:15], v[74:77]
	v_mfma_f32_16x16x32_bf16 v[78:81], v[228:231], v[56:59], v[78:81]
	ds_read_b128 v[220:223], v252 offset:24576
	v_add_u32_e32 v82, v180, v155
	s_waitcnt lgkmcnt(5)
	v_mfma_f32_16x16x32_bf16 v[74:77], v[232:235], v[16:19], v[74:77]
	v_mfma_f32_16x16x32_bf16 v[78:81], v[232:235], v[52:55], v[78:81]
	ds_read_b128 v[224:227], v253 offset:24576
	v_add_u32_e32 v86, v180, v156
	s_waitcnt lgkmcnt(5)
	v_mfma_f32_16x16x32_bf16 v[74:77], v[236:239], v[20:23], v[74:77]
	v_mfma_f32_16x16x32_bf16 v[78:81], v[236:239], v[48:51], v[78:81]
	ds_read_b128 v[228:231], v254 offset:24576
	v_add_u32_e32 v82, v180, v157
	s_waitcnt lgkmcnt(5)
	v_mfma_f32_16x16x32_bf16 v[74:77], v[240:243], v[24:27], v[74:77]
	v_mfma_f32_16x16x32_bf16 v[78:81], v[240:243], v[44:47], v[78:81]
	ds_read_b128 v[232:235], v255 offset:24576
	v_add_u32_e32 v86, v180, v158
	s_waitcnt lgkmcnt(5)
	v_mfma_f32_16x16x32_bf16 v[74:77], v[244:247], v[28:31], v[74:77]
	v_mfma_f32_16x16x32_bf16 v[78:81], v[244:247], v[40:43], v[78:81]
	ds_read_b128 v[236:239], v252 offset:24832
	v_add_u32_e32 v82, v181, v151
	s_waitcnt lgkmcnt(5)
	v_mfma_f32_16x16x32_bf16 v[74:77], v[248:251], v[32:35], v[74:77]
	v_mfma_f32_16x16x32_bf16 v[78:81], v[248:251], v[36:39], v[78:81]
	ds_read_b128 v[240:243], v253 offset:24832
	v_add_u32_e32 v86, v181, v152
	s_nop 5
	v_pk_mul_f32 v[74:75], v[74:75], v[136:137]
	v_pk_mul_f32 v[76:77], v[76:77], v[136:137]
	v_cvt_pk_bf16_f32 v74, v74, v75
	v_cvt_pk_bf16_f32 v75, v76, v77
	v_pk_mul_f32 v[76:77], v[78:79], v[68:69]
	v_pk_mul_f32 v[78:79], v[80:81], v[68:69]
	v_cvt_pk_bf16_f32 v76, v76, v77
	v_cvt_pk_bf16_f32 v77, v78, v79
	global_store_dwordx2 v[70:71], v[74:75], off offset:320
	global_store_dwordx2 v[72:73], v[76:77], off offset:320
	v_mov_b64_e32 v[76:77], v[2:3]
	v_mov_b64_e32 v[80:81], v[2:3]
	v_mov_b64_e32 v[74:75], v[0:1]
	v_mov_b64_e32 v[78:79], v[0:1]
	s_waitcnt lgkmcnt(5)
	v_mfma_f32_16x16x32_bf16 v[74:77], v[220:223], v[4:7], v[74:77]
	v_mfma_f32_16x16x32_bf16 v[78:81], v[220:223], v[64:67], v[78:81]
	ds_read_b128 v[244:247], v254 offset:24832
	v_add_u32_e32 v82, v181, v153
	s_waitcnt lgkmcnt(5)
	v_mfma_f32_16x16x32_bf16 v[74:77], v[224:227], v[8:11], v[74:77]
	v_mfma_f32_16x16x32_bf16 v[78:81], v[224:227], v[60:63], v[78:81]
	ds_read_b128 v[248:251], v255 offset:24832
	v_add_u32_e32 v86, v181, v154
	s_waitcnt lgkmcnt(5)
	v_mfma_f32_16x16x32_bf16 v[74:77], v[228:231], v[12:15], v[74:77]
	v_mfma_f32_16x16x32_bf16 v[78:81], v[228:231], v[56:59], v[78:81]
	ds_read_b128 v[220:223], v252 offset:32768
	v_add_u32_e32 v82, v181, v155
	s_waitcnt lgkmcnt(5)
	v_mfma_f32_16x16x32_bf16 v[74:77], v[232:235], v[16:19], v[74:77]
	v_mfma_f32_16x16x32_bf16 v[78:81], v[232:235], v[52:55], v[78:81]
	ds_read_b128 v[224:227], v253 offset:32768
	v_add_u32_e32 v86, v181, v156
	s_waitcnt lgkmcnt(5)
	v_mfma_f32_16x16x32_bf16 v[74:77], v[236:239], v[20:23], v[74:77]
	v_mfma_f32_16x16x32_bf16 v[78:81], v[236:239], v[48:51], v[78:81]
	ds_read_b128 v[228:231], v254 offset:32768
	v_add_u32_e32 v82, v181, v157
	s_waitcnt lgkmcnt(5)
	v_mfma_f32_16x16x32_bf16 v[74:77], v[240:243], v[24:27], v[74:77]
	v_mfma_f32_16x16x32_bf16 v[78:81], v[240:243], v[44:47], v[78:81]
	ds_read_b128 v[232:235], v255 offset:32768
	v_add_u32_e32 v86, v181, v158
	s_waitcnt lgkmcnt(5)
	v_mfma_f32_16x16x32_bf16 v[74:77], v[244:247], v[28:31], v[74:77]
	v_mfma_f32_16x16x32_bf16 v[78:81], v[244:247], v[40:43], v[78:81]
	ds_read_b128 v[236:239], v252 offset:33024
	v_add_u32_e32 v82, v182, v151
	s_waitcnt lgkmcnt(5)
	v_mfma_f32_16x16x32_bf16 v[74:77], v[248:251], v[32:35], v[74:77]
	v_mfma_f32_16x16x32_bf16 v[78:81], v[248:251], v[36:39], v[78:81]
	ds_read_b128 v[240:243], v253 offset:33024
	v_add_u32_e32 v86, v182, v152
	s_nop 5
	v_pk_mul_f32 v[74:75], v[74:75], v[136:137]
	v_pk_mul_f32 v[76:77], v[76:77], v[136:137]
	v_cvt_pk_bf16_f32 v74, v74, v75
	v_cvt_pk_bf16_f32 v75, v76, v77
	v_pk_mul_f32 v[76:77], v[78:79], v[68:69]
	v_pk_mul_f32 v[78:79], v[80:81], v[68:69]
	v_cvt_pk_bf16_f32 v76, v76, v77
	v_cvt_pk_bf16_f32 v77, v78, v79
	global_store_dwordx2 v[70:71], v[74:75], off offset:352
	global_store_dwordx2 v[72:73], v[76:77], off offset:352
	v_mov_b64_e32 v[76:77], v[2:3]
	v_mov_b64_e32 v[80:81], v[2:3]
	v_mov_b64_e32 v[74:75], v[0:1]
	v_mov_b64_e32 v[78:79], v[0:1]
	s_waitcnt lgkmcnt(5)
	v_mfma_f32_16x16x32_bf16 v[74:77], v[220:223], v[4:7], v[74:77]
	v_mfma_f32_16x16x32_bf16 v[78:81], v[220:223], v[64:67], v[78:81]
	ds_read_b128 v[244:247], v254 offset:33024
	v_add_u32_e32 v82, v182, v153
	s_waitcnt lgkmcnt(5)
	v_mfma_f32_16x16x32_bf16 v[74:77], v[224:227], v[8:11], v[74:77]
	v_mfma_f32_16x16x32_bf16 v[78:81], v[224:227], v[60:63], v[78:81]
	ds_read_b128 v[248:251], v255 offset:33024
	v_add_u32_e32 v86, v182, v154
	s_waitcnt lgkmcnt(5)
	v_mfma_f32_16x16x32_bf16 v[74:77], v[228:231], v[12:15], v[74:77]
	v_mfma_f32_16x16x32_bf16 v[78:81], v[228:231], v[56:59], v[78:81]
	ds_read_b128 v[220:223], v252 offset:40960
	v_add_u32_e32 v82, v182, v155
	s_waitcnt lgkmcnt(5)
	v_mfma_f32_16x16x32_bf16 v[74:77], v[232:235], v[16:19], v[74:77]
	v_mfma_f32_16x16x32_bf16 v[78:81], v[232:235], v[52:55], v[78:81]
	ds_read_b128 v[224:227], v253 offset:40960
	v_add_u32_e32 v86, v182, v156
	s_waitcnt lgkmcnt(5)
	v_mfma_f32_16x16x32_bf16 v[74:77], v[236:239], v[20:23], v[74:77]
	v_mfma_f32_16x16x32_bf16 v[78:81], v[236:239], v[48:51], v[78:81]
	ds_read_b128 v[228:231], v254 offset:40960
	v_add_u32_e32 v82, v182, v157
	s_waitcnt lgkmcnt(5)
	v_mfma_f32_16x16x32_bf16 v[74:77], v[240:243], v[24:27], v[74:77]
	v_mfma_f32_16x16x32_bf16 v[78:81], v[240:243], v[44:47], v[78:81]
	ds_read_b128 v[232:235], v255 offset:40960
	v_add_u32_e32 v86, v182, v158
	s_waitcnt lgkmcnt(5)
	v_mfma_f32_16x16x32_bf16 v[74:77], v[244:247], v[28:31], v[74:77]
	v_mfma_f32_16x16x32_bf16 v[78:81], v[244:247], v[40:43], v[78:81]
	ds_read_b128 v[236:239], v252 offset:41216
	v_add_u32_e32 v82, v183, v151
	s_waitcnt lgkmcnt(5)
	v_mfma_f32_16x16x32_bf16 v[74:77], v[248:251], v[32:35], v[74:77]
	v_mfma_f32_16x16x32_bf16 v[78:81], v[248:251], v[36:39], v[78:81]
	ds_read_b128 v[240:243], v253 offset:41216
	v_add_u32_e32 v86, v183, v152
	s_nop 5
	v_pk_mul_f32 v[74:75], v[74:75], v[136:137]
	v_pk_mul_f32 v[76:77], v[76:77], v[136:137]
	v_cvt_pk_bf16_f32 v74, v74, v75
	v_cvt_pk_bf16_f32 v75, v76, v77
	v_pk_mul_f32 v[76:77], v[78:79], v[68:69]
	v_pk_mul_f32 v[78:79], v[80:81], v[68:69]
	v_cvt_pk_bf16_f32 v76, v76, v77
	v_cvt_pk_bf16_f32 v77, v78, v79
	global_store_dwordx2 v[70:71], v[74:75], off offset:384
	global_store_dwordx2 v[72:73], v[76:77], off offset:384
	v_mov_b64_e32 v[76:77], v[2:3]
	v_mov_b64_e32 v[80:81], v[2:3]
	v_mov_b64_e32 v[74:75], v[0:1]
	v_mov_b64_e32 v[78:79], v[0:1]
	s_waitcnt lgkmcnt(5)
	v_mfma_f32_16x16x32_bf16 v[74:77], v[220:223], v[4:7], v[74:77]
	v_mfma_f32_16x16x32_bf16 v[78:81], v[220:223], v[64:67], v[78:81]
	ds_read_b128 v[244:247], v254 offset:41216
	v_add_u32_e32 v82, v183, v153
	s_waitcnt lgkmcnt(5)
	v_mfma_f32_16x16x32_bf16 v[74:77], v[224:227], v[8:11], v[74:77]
	v_mfma_f32_16x16x32_bf16 v[78:81], v[224:227], v[60:63], v[78:81]
	ds_read_b128 v[248:251], v255 offset:41216
	v_add_u32_e32 v86, v183, v154
	s_waitcnt lgkmcnt(5)
	v_mfma_f32_16x16x32_bf16 v[74:77], v[228:231], v[12:15], v[74:77]
	v_mfma_f32_16x16x32_bf16 v[78:81], v[228:231], v[56:59], v[78:81]
	ds_read_b128 v[220:223], v252 offset:49152
	v_add_u32_e32 v82, v183, v155
	s_waitcnt lgkmcnt(5)
	v_mfma_f32_16x16x32_bf16 v[74:77], v[232:235], v[16:19], v[74:77]
	v_mfma_f32_16x16x32_bf16 v[78:81], v[232:235], v[52:55], v[78:81]
	ds_read_b128 v[224:227], v253 offset:49152
	v_add_u32_e32 v86, v183, v156
	s_waitcnt lgkmcnt(5)
	v_mfma_f32_16x16x32_bf16 v[74:77], v[236:239], v[20:23], v[74:77]
	v_mfma_f32_16x16x32_bf16 v[78:81], v[236:239], v[48:51], v[78:81]
	ds_read_b128 v[228:231], v254 offset:49152
	v_add_u32_e32 v82, v183, v157
	s_waitcnt lgkmcnt(5)
	v_mfma_f32_16x16x32_bf16 v[74:77], v[240:243], v[24:27], v[74:77]
	v_mfma_f32_16x16x32_bf16 v[78:81], v[240:243], v[44:47], v[78:81]
	ds_read_b128 v[232:235], v255 offset:49152
	v_add_u32_e32 v86, v183, v158
	s_waitcnt lgkmcnt(5)
	v_mfma_f32_16x16x32_bf16 v[74:77], v[244:247], v[28:31], v[74:77]
	v_mfma_f32_16x16x32_bf16 v[78:81], v[244:247], v[40:43], v[78:81]
	ds_read_b128 v[236:239], v252 offset:49408
	v_add_u32_e32 v82, v184, v151
	s_waitcnt lgkmcnt(5)
	v_mfma_f32_16x16x32_bf16 v[74:77], v[248:251], v[32:35], v[74:77]
	v_mfma_f32_16x16x32_bf16 v[78:81], v[248:251], v[36:39], v[78:81]
	ds_read_b128 v[240:243], v253 offset:49408
	v_add_u32_e32 v86, v184, v152
	s_nop 5
	v_pk_mul_f32 v[74:75], v[74:75], v[136:137]
	v_pk_mul_f32 v[76:77], v[76:77], v[136:137]
	v_cvt_pk_bf16_f32 v74, v74, v75
	v_cvt_pk_bf16_f32 v75, v76, v77
	v_pk_mul_f32 v[76:77], v[78:79], v[68:69]
	v_pk_mul_f32 v[78:79], v[80:81], v[68:69]
	v_cvt_pk_bf16_f32 v76, v76, v77
	v_cvt_pk_bf16_f32 v77, v78, v79
	global_store_dwordx2 v[70:71], v[74:75], off offset:416
	global_store_dwordx2 v[72:73], v[76:77], off offset:416
	v_mov_b64_e32 v[76:77], v[2:3]
	v_mov_b64_e32 v[80:81], v[2:3]
	v_mov_b64_e32 v[74:75], v[0:1]
	v_mov_b64_e32 v[78:79], v[0:1]
	s_waitcnt lgkmcnt(5)
	v_mfma_f32_16x16x32_bf16 v[74:77], v[220:223], v[4:7], v[74:77]
	v_mfma_f32_16x16x32_bf16 v[78:81], v[220:223], v[64:67], v[78:81]
	ds_read_b128 v[244:247], v254 offset:49408
	v_add_u32_e32 v82, v184, v153
	s_waitcnt lgkmcnt(5)
	v_mfma_f32_16x16x32_bf16 v[74:77], v[224:227], v[8:11], v[74:77]
	v_mfma_f32_16x16x32_bf16 v[78:81], v[224:227], v[60:63], v[78:81]
	ds_read_b128 v[248:251], v255 offset:49408
	v_add_u32_e32 v86, v184, v154
	s_waitcnt lgkmcnt(5)
	v_mfma_f32_16x16x32_bf16 v[74:77], v[228:231], v[12:15], v[74:77]
	v_mfma_f32_16x16x32_bf16 v[78:81], v[228:231], v[56:59], v[78:81]
	v_add_u32_e32 v82, v184, v155
	s_waitcnt lgkmcnt(4)
	v_mfma_f32_16x16x32_bf16 v[74:77], v[232:235], v[16:19], v[74:77]
	v_mfma_f32_16x16x32_bf16 v[78:81], v[232:235], v[52:55], v[78:81]
	v_add_u32_e32 v86, v184, v156
	s_waitcnt lgkmcnt(3)
	v_mfma_f32_16x16x32_bf16 v[74:77], v[236:239], v[20:23], v[74:77]
	v_mfma_f32_16x16x32_bf16 v[78:81], v[236:239], v[48:51], v[78:81]
	v_add_u32_e32 v82, v184, v157
	s_waitcnt lgkmcnt(2)
	v_mfma_f32_16x16x32_bf16 v[74:77], v[240:243], v[24:27], v[74:77]
	v_mfma_f32_16x16x32_bf16 v[78:81], v[240:243], v[44:47], v[78:81]
	v_add_u32_e32 v86, v184, v158
	s_waitcnt lgkmcnt(1)
	v_mfma_f32_16x16x32_bf16 v[74:77], v[244:247], v[28:31], v[74:77]
	v_mfma_f32_16x16x32_bf16 v[78:81], v[244:247], v[40:43], v[78:81]
	v_add_u32_e32 v82, v185, v151
	s_waitcnt lgkmcnt(0)
	v_mfma_f32_16x16x32_bf16 v[74:77], v[248:251], v[32:35], v[74:77]
	v_mfma_f32_16x16x32_bf16 v[78:81], v[248:251], v[36:39], v[78:81]
	v_add_u32_e32 v86, v185, v152
	s_nop 5
	v_pk_mul_f32 v[74:75], v[74:75], v[136:137]
	v_pk_mul_f32 v[76:77], v[76:77], v[136:137]
	v_cvt_pk_bf16_f32 v74, v74, v75
	v_cvt_pk_bf16_f32 v75, v76, v77
	v_pk_mul_f32 v[76:77], v[78:79], v[68:69]
	v_pk_mul_f32 v[78:79], v[80:81], v[68:69]
	v_cvt_pk_bf16_f32 v76, v76, v77
	v_cvt_pk_bf16_f32 v77, v78, v79
	global_store_dwordx2 v[70:71], v[74:75], off offset:448
	global_store_dwordx2 v[72:73], v[76:77], off offset:448
	v_mov_b64_e32 v[76:77], v[2:3]
	v_mov_b64_e32 v[80:81], v[2:3]
	v_mov_b64_e32 v[74:75], v[0:1]
	v_mov_b64_e32 v[78:79], v[0:1]
	ds_read_b128 v[82:85], v82
	ds_read_b128 v[86:89], v86
	s_waitcnt lgkmcnt(1)
	v_mfma_f32_16x16x32_bf16 v[4:7], v[82:85], v[4:7], v[74:77]
	v_mfma_f32_16x16x32_bf16 v[64:67], v[82:85], v[64:67], v[78:81]
	s_waitcnt lgkmcnt(0)
	v_mfma_f32_16x16x32_bf16 v[4:7], v[86:89], v[8:11], v[4:7]
	v_mfma_f32_16x16x32_bf16 v[8:11], v[86:89], v[60:63], v[64:67]
	v_add_u32_e32 v60, v185, v153
	ds_read_b128 v[60:63], v60
	s_nop 2
	v_add_u32_e32 v64, v185, v154
	ds_read_b128 v[64:67], v64
	s_waitcnt lgkmcnt(1)
	v_mfma_f32_16x16x32_bf16 v[4:7], v[60:63], v[12:15], v[4:7]
	v_add_u32_e32 v12, v185, v155
	ds_read_b128 v[12:15], v12
	v_mfma_f32_16x16x32_bf16 v[8:11], v[60:63], v[56:59], v[8:11]
	s_waitcnt lgkmcnt(1)
	v_mfma_f32_16x16x32_bf16 v[4:7], v[64:67], v[16:19], v[4:7]
	v_add_u32_e32 v16, v185, v156
	ds_read_b128 v[16:19], v16
	v_mfma_f32_16x16x32_bf16 v[8:11], v[64:67], v[52:55], v[8:11]
	s_waitcnt lgkmcnt(1)
	v_mfma_f32_16x16x32_bf16 v[4:7], v[12:15], v[20:23], v[4:7]
	v_add_u32_e32 v20, v185, v158
	v_mfma_f32_16x16x32_bf16 v[8:11], v[12:15], v[48:51], v[8:11]
	v_add_u32_e32 v12, v185, v157
	ds_read_b128 v[12:15], v12
	s_waitcnt lgkmcnt(1)
	v_mfma_f32_16x16x32_bf16 v[4:7], v[16:19], v[24:27], v[4:7]
	v_mfma_f32_16x16x32_bf16 v[8:11], v[16:19], v[44:47], v[8:11]
	ds_read_b128 v[16:19], v20
	s_waitcnt lgkmcnt(1)
	v_mfma_f32_16x16x32_bf16 v[4:7], v[12:15], v[28:31], v[4:7]
	s_waitcnt lgkmcnt(0)
	v_mfma_f32_16x16x32_bf16 v[4:7], v[16:19], v[32:35], v[4:7]
	v_mfma_f32_16x16x32_bf16 v[8:11], v[12:15], v[40:43], v[8:11]
	s_nop 6
	v_mul_f32_e64 v4, v4, v136
	v_mul_f32_e64 v5, v5, v137
	v_cvt_pk_bf16_f32 v12, v4, v5
	v_pk_mul_f32 v[4:5], v[6:7], v[136:137]
	s_nop 0
	v_cvt_pk_bf16_f32 v13, v4, v5
	v_mfma_f32_16x16x32_bf16 v[4:7], v[16:19], v[36:39], v[8:11]
	s_nop 7
	v_pk_mul_f32 v[4:5], v[4:5], v[68:69]
	v_pk_mul_f32 v[6:7], v[6:7], v[68:69]
	v_cvt_pk_bf16_f32 v4, v4, v5
	v_cvt_pk_bf16_f32 v5, v6, v7
	global_store_dwordx2 v[70:71], v[12:13], off offset:480
	global_store_dwordx2 v[72:73], v[4:5], off offset:480
	s_waitcnt lgkmcnt(0)
	s_barrier
	s_cbranch_vccz .LBB0_1066
	s_mov_b32 m0, s50
	s_mov_b64 s[2:3], 0
	buffer_load_dwordx4 v140, s[12:15], s49 offen lds
	s_mov_b32 m0, s51
	s_nop 0
	buffer_load_dwordx4 v141, s[12:15], s49 offen lds
	s_mov_b32 m0, s52
	s_nop 0
	buffer_load_dwordx4 v142, s[12:15], s49 offen lds
	s_mov_b32 m0, s53
	s_nop 0
	buffer_load_dwordx4 v143, s[12:15], s49 offen lds
	s_mov_b32 m0, s54
	s_nop 0
	buffer_load_dwordx4 v144, s[12:15], s49 offen lds
	s_mov_b32 m0, s55
	s_nop 0
	buffer_load_dwordx4 v145, s[12:15], s49 offen lds
	s_mov_b32 m0, s56
	s_nop 0
	buffer_load_dwordx4 v146, s[12:15], s49 offen lds
	s_mov_b32 m0, s57
	s_nop 0
	buffer_load_dwordx4 v147, s[12:15], s49 offen lds
	s_branch .LBB0_1066

	.amdhsa_kernel _Z9hymba_fwd4Args
		.amdhsa_group_segment_fixed_size 0
		.amdhsa_private_segment_fixed_size 0
		.amdhsa_kernarg_size 560
		.amdhsa_user_sgpr_count 2
		.amdhsa_user_sgpr_dispatch_ptr 0
		.amdhsa_user_sgpr_queue_ptr 0
		.amdhsa_user_sgpr_kernarg_segment_ptr 1
		.amdhsa_user_sgpr_dispatch_id 0
		.amdhsa_user_sgpr_kernarg_preload_length 0
		.amdhsa_user_sgpr_kernarg_preload_offset 0
		.amdhsa_user_sgpr_private_segment_size 0
		.amdhsa_uses_dynamic_stack 0
		.amdhsa_enable_private_segment 0
		.amdhsa_system_sgpr_workgroup_id_x 1
		.amdhsa_system_sgpr_workgroup_id_y 0
		.amdhsa_system_sgpr_workgroup_id_z 0
		.amdhsa_system_sgpr_workgroup_info 0
		.amdhsa_system_vgpr_workitem_id 0
		.amdhsa_next_free_vgpr 256
		.amdhsa_next_free_sgpr 101
		.amdhsa_accum_offset 256
		.amdhsa_reserve_vcc 1
		.amdhsa_float_round_mode_32 0
		.amdhsa_float_round_mode_16_64 0
		.amdhsa_float_denorm_mode_32 3
		.amdhsa_float_denorm_mode_16_64 3
		.amdhsa_dx10_clamp 1
		.amdhsa_ieee_mode 1
		.amdhsa_fp16_overflow 0
		.amdhsa_tg_split 0
		.amdhsa_exception_fp_ieee_invalid_op 0
		.amdhsa_exception_fp_denorm_src 0
		.amdhsa_exception_fp_ieee_div_zero 0
		.amdhsa_exception_fp_ieee_overflow 0
		.amdhsa_exception_fp_ieee_underflow 0
		.amdhsa_exception_fp_ieee_inexact 0
		.amdhsa_exception_int_div_zero 0
	.end_amdhsa_kernel

amdhsa.kernels:
  - .agpr_count:     0
    .args:
      - .offset:         0
        .size:           304
        .value_kind:     by_value
      - .offset:         304
        .size:           4
        .value_kind:     hidden_block_count_x
      - .offset:         308
        .size:           4
        .value_kind:     hidden_block_count_y
      - .offset:         312
        .size:           4
        .value_kind:     hidden_block_count_z
      - .offset:         316
        .size:           2
        .value_kind:     hidden_group_size_x
      - .offset:         318
        .size:           2
        .value_kind:     hidden_group_size_y
      - .offset:         320
        .size:           2
        .value_kind:     hidden_group_size_z
      - .offset:         322
        .size:           2
        .value_kind:     hidden_remainder_x
      - .offset:         324
        .size:           2
        .value_kind:     hidden_remainder_y
      - .offset:         326
        .size:           2
        .value_kind:     hidden_remainder_z
      - .offset:         344
        .size:           8
        .value_kind:     hidden_global_offset_x
      - .offset:         352
        .size:           8
        .value_kind:     hidden_global_offset_y
      - .offset:         360
        .size:           8
        .value_kind:     hidden_global_offset_z
      - .offset:         368
        .size:           2
        .value_kind:     hidden_grid_dims
      - .offset:         424
        .size:           4
        .value_kind:     hidden_dynamic_lds_size
    .group_segment_fixed_size: 0
    .kernarg_segment_align: 8
    .kernarg_segment_size: 560
    .language:       OpenCL C
    .language_version:
      - 2
      - 0
    .max_flat_workgroup_size: 512
    .name:           _Z9hymba_fwd4Args
    .private_segment_fixed_size: 0
    .sgpr_count:     107
    .sgpr_spill_count: 18
    .symbol:         _Z9hymba_fwd4Args.kd
    .uniform_work_group_size: 1
    .uses_dynamic_stack: false
    .vgpr_count:     256
    .vgpr_spill_count: 0
    .wavefront_size: 64
